# adds: context hyena conv guarded loads batched (64 and 32 loads in flight instead of 16 serial groups)
# baseline (speedup 1.0000x reference)
; #define LAS __attribute__((address_space(3)))
; __device__ __forceinline__ void lds_barrier() { asm volatile("s_waitcnt lgkmcnt(0)" ::: "memory"); __builtin_amdgcn_s_barrier(); asm volatile("" ::: "memory"); }
; template <bool LAT>
; __device__ __forceinline__ void hyconv_unit(const Frame& F, LAS f32x2v* X, const TwHalf tw, LAS bf16* OUT, const float* skip, bf16* MIX, int u) {
;     ...
;     for (int ci = 0; ci < nci; ++ci) {
;         const int c0 = cbase + ci;
;         const f32x2v* SPb = (const f32x2v*)(F.ws + (LAT ? WS_SPEC : WS_SPECC)) + (size_t)c0 * N;
;         lds_barrier();
;         if constexpr (LAT) {
;             unsigned w0[4], w1[4]; const bf16* p0 = H0 + (size_t)(512 + c0) * L; const bf16* p1 = H1 + (size_t)(512 + c0) * L;
; #pragma unroll
;             for (int r = 0; r < 4; ++r) { const int pr = F.tid + 512 * r; w0[r] = *(const unsigned*)(p0 + 2 * pr); w1[r] = *(const unsigned*)(p1 + 2 * pr); }
; #pragma unroll
;             for (int r = 0; r < 8; ++r) { const int e = 2 * (F.tid + 512 * r); f32x4 xx = (f32x4){0.f, 0.f, 0.f, 0.f};
;                 if (r < 4) xx = (f32x4){bflo(w0[r]), bflo(w1[r]), bfhi(w0[r]), bfhi(w1[r])};
;                 *(LAS f32x4*)(X + PADI(e)) = xx; }
;         } else {
;             f32x2v v[16];
;             { const bf16* p0 = H0 + (size_t)(512 + c0) * L + n; const bf16* p1 = H1 + (size_t)(512 + c0) * L + n;
; #pragma unroll
;               for (int r = 0; r < 16; ++r) { v[r] = (f32x2v){0.f, 0.f}; if (act) v[r] = (f32x2v){bf2f(p0[r * L]), bf2f(p1[r * L])}; } }
; #pragma unroll
;             for (int r = 0; r < 16; ++r) X[PADI(F.tid + 512 * r)] = v[r];
;         }
;         lds_barrier();
.LBB0_812:
	s_add_i32 s0, s23, 0xffffff00
	s_ashr_i32 s0, s0, 3
	s_lshl_b32 s1, s23, 4
	s_and_b32 s14, s0, -2
	s_and_b32 s24, s1, 0xf0
	s_mul_i32 s1, s14, 0x60000
	s_mul_hi_i32 s0, s14, 0x60000
	s_add_u32 s2, s16, s1
	s_addc_u32 s3, s17, s0
	s_add_u32 s0, s2, 0x60000
	s_addc_u32 s1, s3, 0
	s_lshl_b32 s4, s24, 9
	s_or_b32 s15, s4, 0x40000
	s_add_u32 s4, s2, s15
	s_addc_u32 s5, s3, 0
	v_lshl_add_u64 v[52:53], s[4:5], 0, v[50:51]
	s_add_u32 s4, s0, s15
	s_waitcnt lgkmcnt(0)
	s_barrier
	s_addc_u32 s5, s1, 0
	v_lshl_add_u64 v[54:55], s[4:5], 0, v[50:51]
	v_mov_b32_e32 v2, 0
	v_mov_b32_e32 v3, 0
	v_mov_b32_e32 v0, 0
	v_mov_b32_e32 v1, 0
	v_mov_b32_e32 v6, 0
	v_mov_b32_e32 v7, 0
	v_mov_b32_e32 v4, 0
	v_mov_b32_e32 v5, 0
	v_mov_b32_e32 v10, 0
	v_mov_b32_e32 v11, 0
	v_mov_b32_e32 v8, 0
	v_mov_b32_e32 v9, 0
	v_mov_b32_e32 v14, 0
	v_mov_b32_e32 v15, 0
	v_mov_b32_e32 v12, 0
	v_mov_b32_e32 v13, 0
	v_mov_b32_e32 v18, 0
	v_mov_b32_e32 v19, 0
	v_mov_b32_e32 v16, 0
	v_mov_b32_e32 v17, 0
	v_mov_b32_e32 v22, 0
	v_mov_b32_e32 v23, 0
	v_mov_b32_e32 v20, 0
	v_mov_b32_e32 v21, 0
	v_mov_b32_e32 v26, 0
	v_mov_b32_e32 v27, 0
	v_mov_b32_e32 v24, 0
	v_mov_b32_e32 v25, 0
	v_mov_b32_e32 v30, 0
	v_mov_b32_e32 v31, 0
	v_mov_b32_e32 v28, 0
	v_mov_b32_e32 v29, 0
	s_and_saveexec_b64 s[4:5], s[38:39]
	v_add_co_u32_e32 v192, vcc, 0x1000, v52
	s_nop 1
	v_addc_co_u32_e32 v193, vcc, 0, v53, vcc
	v_add_co_u32_e32 v194, vcc, 0x1000, v54
	s_nop 1
	v_addc_co_u32_e32 v195, vcc, 0, v55, vcc
	global_load_ushort v2, v[52:53], off
	global_load_ushort v3, v[54:55], off
	global_load_ushort v0, v[52:53], off offset:512
	global_load_ushort v1, v[54:55], off offset:512
	global_load_ushort v6, v[52:53], off offset:1024
	global_load_ushort v7, v[54:55], off offset:1024
	global_load_ushort v4, v[52:53], off offset:1536
	global_load_ushort v5, v[54:55], off offset:1536
	global_load_ushort v10, v[52:53], off offset:2048
	global_load_ushort v11, v[54:55], off offset:2048
	global_load_ushort v8, v[52:53], off offset:2560
	global_load_ushort v9, v[54:55], off offset:2560
	global_load_ushort v14, v[52:53], off offset:3072
	global_load_ushort v15, v[54:55], off offset:3072
	global_load_ushort v12, v[52:53], off offset:3584
	global_load_ushort v13, v[54:55], off offset:3584
	global_load_ushort v18, v[192:193], off
	global_load_ushort v19, v[194:195], off
	global_load_ushort v16, v[192:193], off offset:512
	global_load_ushort v17, v[194:195], off offset:512
	global_load_ushort v22, v[192:193], off offset:1024
	global_load_ushort v23, v[194:195], off offset:1024
	global_load_ushort v20, v[192:193], off offset:1536
	global_load_ushort v21, v[194:195], off offset:1536
	global_load_ushort v26, v[192:193], off offset:2048
	global_load_ushort v27, v[194:195], off offset:2048
	global_load_ushort v24, v[192:193], off offset:2560
	global_load_ushort v25, v[194:195], off offset:2560
	global_load_ushort v30, v[192:193], off offset:3072
	global_load_ushort v31, v[194:195], off offset:3072
	global_load_ushort v28, v[192:193], off offset:3584
	global_load_ushort v29, v[194:195], off offset:3584
	s_waitcnt vmcnt(0)
	v_lshlrev_b32_e32 v2, 16, v2
	v_lshlrev_b32_e32 v3, 16, v3
	v_lshlrev_b32_e32 v0, 16, v0
	v_lshlrev_b32_e32 v1, 16, v1
	v_lshlrev_b32_e32 v6, 16, v6
	v_lshlrev_b32_e32 v7, 16, v7
	v_lshlrev_b32_e32 v4, 16, v4
	v_lshlrev_b32_e32 v5, 16, v5
	v_lshlrev_b32_e32 v10, 16, v10
	v_lshlrev_b32_e32 v11, 16, v11
	v_lshlrev_b32_e32 v8, 16, v8
	v_lshlrev_b32_e32 v9, 16, v9
	v_lshlrev_b32_e32 v14, 16, v14
	v_lshlrev_b32_e32 v15, 16, v15
	v_lshlrev_b32_e32 v12, 16, v12
	v_lshlrev_b32_e32 v13, 16, v13
	v_lshlrev_b32_e32 v18, 16, v18
	v_lshlrev_b32_e32 v19, 16, v19
	v_lshlrev_b32_e32 v16, 16, v16
	v_lshlrev_b32_e32 v17, 16, v17
	v_lshlrev_b32_e32 v22, 16, v22
	v_lshlrev_b32_e32 v23, 16, v23
	v_lshlrev_b32_e32 v20, 16, v20
	v_lshlrev_b32_e32 v21, 16, v21
	v_lshlrev_b32_e32 v26, 16, v26
	v_lshlrev_b32_e32 v27, 16, v27
	v_lshlrev_b32_e32 v24, 16, v24
	v_lshlrev_b32_e32 v25, 16, v25
	v_lshlrev_b32_e32 v30, 16, v30
	v_lshlrev_b32_e32 v31, 16, v31
	v_lshlrev_b32_e32 v28, 16, v28
	v_lshlrev_b32_e32 v29, 16, v29
	s_or_b64 exec, exec, s[4:5]
	s_lshl_b32 s4, s24, 12
	v_lshl_add_u64 v[56:57], s[2:3], 0, v[50:51]
	s_lshl_b32 s2, s24, 1
	v_lshl_add_u32 v58, s14, 8, v138
	s_add_u32 s2, s12, s2
	v_ashrrev_i32_e32 v59, 31, v58
	s_addc_u32 s3, s13, 0
	v_lshlrev_b64 v[58:59], 11, v[58:59]
	v_lshl_add_u64 v[58:59], s[2:3], 0, v[58:59]
	v_lshl_add_u64 v[62:63], s[0:1], 0, v[50:51]
	s_mov_b64 s[0:1], 0x80010
	v_lshl_add_u64 v[64:65], v[58:59], 0, s[0:1]
	s_mov_b64 s[0:1], 0x1000
	v_lshl_add_u64 v[66:67], v[52:53], 0, s[0:1]
	v_lshl_add_u64 v[68:69], v[54:55], 0, s[0:1]
	s_mov_b64 s[0:1], 0x1200
	v_lshl_add_u64 v[70:71], v[52:53], 0, s[0:1]
	v_lshl_add_u64 v[72:73], v[54:55], 0, s[0:1]
	s_mov_b64 s[0:1], 0x1400
	v_lshl_add_u64 v[74:75], v[52:53], 0, s[0:1]
	v_lshl_add_u64 v[76:77], v[54:55], 0, s[0:1]
	s_mov_b64 s[0:1], 0x1600
	v_lshl_add_u64 v[78:79], v[52:53], 0, s[0:1]
	v_lshl_add_u64 v[80:81], v[54:55], 0, s[0:1]
	s_mov_b64 s[0:1], 0x1800
	ds_write_b64 v140, v[2:3]
	ds_write_b64 v141, v[0:1] offset:4096
	ds_write_b64 v142, v[6:7] offset:8192
	ds_write_b64 v143, v[4:5] offset:12288
	ds_write_b64 v144, v[10:11] offset:16384
	ds_write_b64 v145, v[8:9] offset:20480
	ds_write_b64 v146, v[14:15] offset:24576
	ds_write_b64 v147, v[12:13] offset:28672
	ds_write_b64 v148, v[18:19] offset:32768
	ds_write_b64 v149, v[16:17] offset:36864
	ds_write_b64 v150, v[22:23] offset:40960
	ds_write_b64 v151, v[20:21] offset:45056
	ds_write_b64 v152, v[26:27] offset:49152
	ds_write_b64 v153, v[24:25] offset:53248
	ds_write_b64 v154, v[30:31] offset:57344
	ds_write_b64 v155, v[28:29] offset:61440
	v_lshl_add_u64 v[82:83], v[52:53], 0, s[0:1]
	v_lshl_add_u64 v[84:85], v[54:55], 0, s[0:1]
	s_mov_b64 s[0:1], 0x1a00
	s_waitcnt lgkmcnt(0)
	s_barrier
	v_lshl_add_u64 v[86:87], v[52:53], 0, s[0:1]
	v_lshl_add_u64 v[88:89], v[54:55], 0, s[0:1]
	s_mov_b64 s[0:1], 0x1c00
	s_add_u32 s4, s19, s4
	s_mov_b64 s[2:3], 0x80000
	v_lshl_add_u64 v[90:91], v[52:53], 0, s[0:1]
	v_lshl_add_u64 v[92:93], v[54:55], 0, s[0:1]
	s_mov_b64 s[0:1], 0x1e00
	s_addc_u32 s5, s22, 0
	v_lshl_add_u64 v[60:61], v[58:59], 0, s[2:3]
	v_lshl_add_u64 v[94:95], v[52:53], 0, s[0:1]
	v_lshl_add_u64 v[96:97], v[54:55], 0, s[0:1]
	s_mov_b32 s2, 0
	s_mov_b64 s[20:21], -1
	s_branch .LBB0_847

; template <int R, class XT, class TWT>
; __device__ __forceinline__ void dif_task(XT X, TWT tw, int s, int task) {
;     const int lgM = 13 - s, lgq = lgM - R, q = 1 << lgq;
;     const int j0 = task & (q - 1), blk = task >> lgq, base = (blk << lgM) + j0;
;     const int pb = PADI(base), qp = (q >= 32) ? q + (q >> 4) : q;
;     f32x2v v[1 << R];
; #pragma unroll
;     for (int k = 0; k < (1 << R); ++k) v[k] = X[pb + k * qp];
; #pragma unroll
;     for (int r = 0; r < R; ++r) {
;         const int pb = R - 1 - r;
; #pragma unroll
;         for (int k = 0; k < (1 << R); ++k) if (!((k >> pb) & 1)) {
;             const int klo = k & ((1 << pb) - 1);
;             const f32x2v w = tw[(j0 + (klo << lgq)) << (s + r)];
;             const f32x2v a = v[k], b = v[k + (1 << pb)], d = a - b;
;             v[k] = a + b; v[k + (1 << pb)] = (f32x2v){d.x * w.x - d.y * w.y, d.x * w.y + d.y * w.x};
;         }
;     }
; #pragma unroll
;     for (int k = 0; k < (1 << R); ++k) X[pb + k * qp] = v[k];
; }
; template <bool LAT>
; __device__ __forceinline__ void hyconv_unit(const Frame& F, LAS f32x2v* X, const TwHalf tw, LAS bf16* OUT, const float* skip, bf16* MIX, int u) {
;     ...
;             const f32x2v* SP = SPb + (size_t)ord * 256 * N;
;             f32x4 kq[8];
; #pragma unroll
;             for (int r = 0; r < 8; ++r) kq[r] = *(const f32x4*)(SP + 2 * (F.tid + 512 * r));
;             fft_fwd_upper(X, tw, 13 - lgN, F.tid);
.LBB0_847:
	s_lshl_b32 s90, s2, 17
	s_lshl_b64 s[0:1], s[90:91], 3
	s_add_u32 s0, s4, s0
	s_addc_u32 s1, s5, s1
	v_lshl_add_u64 v[0:1], v[34:35], 3, s[0:1]
	v_lshl_add_u64 v[2:3], v[36:37], 3, s[0:1]
	global_load_dwordx4 v[28:31], v[0:1], off
	global_load_dwordx4 v[24:27], v[2:3], off
	v_lshl_add_u64 v[0:1], v[38:39], 3, s[0:1]
	v_lshl_add_u64 v[2:3], v[40:41], 3, s[0:1]
	global_load_dwordx4 v[20:23], v[0:1], off
	global_load_dwordx4 v[16:19], v[2:3], off
	v_lshl_add_u64 v[0:1], v[42:43], 3, s[0:1]
	v_lshl_add_u64 v[2:3], v[44:45], 3, s[0:1]
	global_load_dwordx4 v[12:15], v[0:1], off
	global_load_dwordx4 v[8:11], v[2:3], off
	v_lshl_add_u64 v[0:1], v[46:47], 3, s[0:1]
	v_lshl_add_u64 v[2:3], v[48:49], 3, s[0:1]
	global_load_dwordx4 v[4:7], v[0:1], off
	s_nop 0
	global_load_dwordx4 v[0:3], v[2:3], off
	ds_read2_b64 v[100:103], v135 offset1:34
	ds_read2_b64 v[104:107], v135 offset0:68 offset1:102
	ds_read2_b64 v[108:111], v135 offset0:136 offset1:170
	ds_read2_b64 v[112:115], v135 offset0:204 offset1:238
	v_add_u32_e32 v98, 0x800, v135
	ds_read2_b64 v[116:119], v98 offset0:16 offset1:50
	ds_read2_b64 v[120:123], v98 offset0:84 offset1:118
	ds_read2_b64 v[124:127], v98 offset0:152 offset1:186
	ds_read2_b64 v[128:131], v98 offset0:220 offset1:254
	ds_read2st64_b64 v[176:179], v33 offset1:16
	ds_read_b64 v[132:133], v165
	ds_read_b64 v[182:183], v166
	ds_read_b64 v[184:185], v167
	ds_read_b64 v[186:187], v168
	ds_read_b64 v[188:189], v169
	ds_read_b64 v[190:191], v139
	ds_read_b64 v[192:193], v136
	s_waitcnt lgkmcnt(11)
	v_pk_add_f32 v[194:195], v[100:101], v[116:117] neg_lo:[0,1] neg_hi:[0,1]
	v_pk_add_f32 v[100:101], v[100:101], v[116:117]
	s_waitcnt lgkmcnt(7)
	v_pk_mul_f32 v[196:197], v[194:195], v[176:177] op_sel:[1,1] op_sel_hi:[1,0]
	s_lshl_b32 s0, s2, 8
	v_pk_fma_f32 v[198:199], v[194:195], v[176:177], v[196:197] neg_lo:[0,0,1] neg_hi:[0,0,1]
	v_pk_fma_f32 v[194:195], v[194:195], v[176:177], v[196:197] op_sel_hi:[0,1,1]
	v_mov_b32_e32 v199, v195
	v_pk_add_f32 v[194:195], v[108:109], v[124:125] neg_lo:[0,1] neg_hi:[0,1]
	v_pk_add_f32 v[108:109], v[108:109], v[124:125]
	v_pk_mul_f32 v[196:197], v[194:195], v[176:177] op_sel:[1,0] op_sel_hi:[0,0]
	v_pk_fma_f32 v[202:203], v[194:195], v[176:177], v[196:197] op_sel:[0,1,0]
	v_pk_fma_f32 v[176:177], v[194:195], v[176:177], v[196:197] op_sel:[0,1,0] neg_lo:[0,0,1] neg_hi:[0,0,1]
	v_pk_add_f32 v[116:117], v[100:101], v[108:109]
	v_mov_b32_e32 v203, v177
	v_pk_add_f32 v[176:177], v[198:199], v[202:203] neg_lo:[0,1] neg_hi:[0,1]
	s_waitcnt lgkmcnt(0)
	v_xor_b32_e32 v99, 0x80000000, v192
	v_pk_mul_f32 v[194:195], v[184:185], v[176:177] op_sel:[1,1] op_sel_hi:[0,1]
	v_pk_fma_f32 v[196:197], v[184:185], v[176:177], v[194:195] neg_lo:[0,0,1] neg_hi:[0,0,1]
	v_pk_fma_f32 v[176:177], v[184:185], v[176:177], v[194:195] op_sel_hi:[1,0,1]
	v_pk_add_f32 v[100:101], v[100:101], v[108:109] neg_lo:[0,1] neg_hi:[0,1]
	v_mov_b32_e32 v197, v177
	v_pk_add_f32 v[176:177], v[104:105], v[120:121] neg_lo:[0,1] neg_hi:[0,1]
	v_pk_add_f32 v[104:105], v[104:105], v[120:121]
	v_pk_mul_f32 v[194:195], v[176:177], v[178:179] op_sel:[1,1] op_sel_hi:[1,0]
	v_pk_mul_f32 v[108:109], v[100:101], v[184:185] op_sel:[1,1] op_sel_hi:[1,0]
	v_pk_fma_f32 v[204:205], v[176:177], v[178:179], v[194:195] neg_lo:[0,0,1] neg_hi:[0,0,1]
	v_pk_fma_f32 v[176:177], v[176:177], v[178:179], v[194:195] op_sel_hi:[0,1,1]
	v_mov_b32_e32 v205, v177
	v_pk_add_f32 v[176:177], v[112:113], v[128:129] neg_lo:[0,1] neg_hi:[0,1]
	v_pk_add_f32 v[112:113], v[112:113], v[128:129]
	v_pk_mul_f32 v[194:195], v[176:177], v[178:179] op_sel:[1,0] op_sel_hi:[0,0]
	v_pk_fma_f32 v[206:207], v[176:177], v[178:179], v[194:195] op_sel:[0,1,0]
	v_pk_fma_f32 v[176:177], v[176:177], v[178:179], v[194:195] op_sel:[0,1,0] neg_lo:[0,0,1] neg_hi:[0,0,1]
	v_pk_add_f32 v[120:121], v[104:105], v[112:113]
	v_mov_b32_e32 v207, v177
	v_pk_add_f32 v[176:177], v[204:205], v[206:207] neg_lo:[0,1] neg_hi:[0,1]
	v_pk_add_f32 v[124:125], v[116:117], v[120:121]
	v_pk_mul_f32 v[178:179], v[184:185], v[176:177] op_sel_hi:[0,1]
	v_pk_fma_f32 v[194:195], v[184:185], v[176:177], v[178:179] op_sel:[1,0,1] op_sel_hi:[1,1,0]
	v_pk_fma_f32 v[176:177], v[184:185], v[176:177], v[178:179] op_sel:[1,0,1] op_sel_hi:[1,1,0] neg_lo:[0,0,1] neg_hi:[0,0,1]
	v_pk_add_f32 v[116:117], v[116:117], v[120:121] neg_lo:[0,1] neg_hi:[0,1]
	v_mov_b32_e32 v195, v177
	v_pk_add_f32 v[176:177], v[196:197], v[194:195] neg_lo:[0,1] neg_hi:[0,1]
	v_pk_mul_f32 v[120:121], v[116:117], v[188:189] op_sel:[1,1] op_sel_hi:[1,0]
	v_pk_mul_f32 v[178:179], v[188:189], v[176:177] op_sel:[1,1] op_sel_hi:[0,1]
	v_pk_fma_f32 v[208:209], v[188:189], v[176:177], v[178:179] neg_lo:[0,0,1] neg_hi:[0,0,1]
	v_pk_fma_f32 v[176:177], v[188:189], v[176:177], v[178:179] op_sel_hi:[1,0,1]
	s_or_b32 s14, s0, s24
	v_mov_b32_e32 v209, v177
	v_pk_add_f32 v[176:177], v[102:103], v[118:119] neg_lo:[0,1] neg_hi:[0,1]
	v_pk_add_f32 v[102:103], v[102:103], v[118:119]
	v_pk_mul_f32 v[178:179], v[176:177], v[132:133] op_sel:[1,1] op_sel_hi:[1,0]
	s_lshl_b32 s90, s14, 9
	v_pk_fma_f32 v[220:221], v[176:177], v[132:133], v[178:179] neg_lo:[0,0,1] neg_hi:[0,0,1]
	v_pk_fma_f32 v[176:177], v[176:177], v[132:133], v[178:179] op_sel_hi:[0,1,1]
	v_mov_b32_e32 v221, v177
	v_pk_add_f32 v[176:177], v[110:111], v[126:127] neg_lo:[0,1] neg_hi:[0,1]
	v_pk_add_f32 v[110:111], v[110:111], v[126:127]
	v_pk_mul_f32 v[178:179], v[176:177], v[132:133] op_sel:[1,0] op_sel_hi:[0,0]
	v_pk_fma_f32 v[222:223], v[176:177], v[132:133], v[178:179] op_sel:[0,1,0]
	v_pk_fma_f32 v[132:133], v[176:177], v[132:133], v[178:179] op_sel:[0,1,0] neg_lo:[0,0,1] neg_hi:[0,0,1]
; template <int R, class XT, class TWT>
; __device__ __forceinline__ void dif_task(XT X, TWT tw, int s, int task) {
;     const int lgM = 13 - s, lgq = lgM - R, q = 1 << lgq;
;     const int j0 = task & (q - 1), blk = task >> lgq, base = (blk << lgM) + j0;
;     const int pb = PADI(base), qp = (q >= 32) ? q + (q >> 4) : q;
;     f32x2v v[1 << R];
; #pragma unroll
;     for (int k = 0; k < (1 << R); ++k) v[k] = X[pb + k * qp];
; #pragma unroll
;     for (int r = 0; r < R; ++r) {
;         const int pb = R - 1 - r;
; #pragma unroll
;         for (int k = 0; k < (1 << R); ++k) if (!((k >> pb) & 1)) {
;             const int klo = k & ((1 << pb) - 1);
;             const f32x2v w = tw[(j0 + (klo << lgq)) << (s + r)];
;             const f32x2v a = v[k], b = v[k + (1 << pb)], d = a - b;
;             v[k] = a + b; v[k + (1 << pb)] = (f32x2v){d.x * w.x - d.y * w.y, d.x * w.y + d.y * w.x};
;         }
;     }
; #pragma unroll
;     for (int k = 0; k < (1 << R); ++k) X[pb + k * qp] = v[k];
; }
	v_pk_add_f32 v[118:119], v[102:103], v[110:111]
	v_mov_b32_e32 v223, v133
	v_pk_add_f32 v[132:133], v[220:221], v[222:223] neg_lo:[0,1] neg_hi:[0,1]
	v_pk_add_f32 v[102:103], v[102:103], v[110:111] neg_lo:[0,1] neg_hi:[0,1]
	v_pk_mul_f32 v[176:177], v[186:187], v[132:133] op_sel:[1,1] op_sel_hi:[0,1]
	v_pk_fma_f32 v[178:179], v[186:187], v[132:133], v[176:177] neg_lo:[0,0,1] neg_hi:[0,0,1]
	v_pk_fma_f32 v[132:133], v[186:187], v[132:133], v[176:177] op_sel_hi:[1,0,1]
	s_nop 0
	v_mov_b32_e32 v179, v133
	v_pk_add_f32 v[132:133], v[106:107], v[122:123] neg_lo:[0,1] neg_hi:[0,1]
	v_pk_add_f32 v[106:107], v[106:107], v[122:123]
	v_pk_mul_f32 v[176:177], v[132:133], v[182:183] op_sel:[1,1] op_sel_hi:[1,0]
	s_nop 0
	v_pk_fma_f32 v[224:225], v[132:133], v[182:183], v[176:177] neg_lo:[0,0,1] neg_hi:[0,0,1]
	v_pk_fma_f32 v[132:133], v[132:133], v[182:183], v[176:177] op_sel_hi:[0,1,1]
	v_mov_b32_e32 v225, v133
	v_pk_add_f32 v[132:133], v[114:115], v[130:131] neg_lo:[0,1] neg_hi:[0,1]
	v_pk_add_f32 v[114:115], v[114:115], v[130:131]
	v_pk_mul_f32 v[176:177], v[132:133], v[182:183] op_sel:[1,0] op_sel_hi:[0,0]
	v_pk_fma_f32 v[226:227], v[132:133], v[182:183], v[176:177] op_sel:[0,1,0]
	v_pk_fma_f32 v[132:133], v[132:133], v[182:183], v[176:177] op_sel:[0,1,0] neg_lo:[0,0,1] neg_hi:[0,0,1]
	v_pk_add_f32 v[122:123], v[106:107], v[114:115]
	v_mov_b32_e32 v227, v133
	v_pk_add_f32 v[132:133], v[224:225], v[226:227] neg_lo:[0,1] neg_hi:[0,1]
	v_pk_add_f32 v[126:127], v[118:119], v[122:123]
	v_pk_mul_f32 v[176:177], v[190:191], v[132:133] op_sel_hi:[0,1]
	v_pk_fma_f32 v[182:183], v[190:191], v[132:133], v[176:177] op_sel:[1,0,1] op_sel_hi:[1,1,0]
	v_pk_fma_f32 v[132:133], v[190:191], v[132:133], v[176:177] op_sel:[1,0,1] op_sel_hi:[1,1,0] neg_lo:[0,0,1] neg_hi:[0,0,1]
	v_pk_add_f32 v[128:129], v[124:125], v[126:127]
	v_mov_b32_e32 v183, v133
	v_pk_add_f32 v[132:133], v[178:179], v[182:183] neg_lo:[0,1] neg_hi:[0,1]
	v_pk_add_f32 v[124:125], v[124:125], v[126:127] neg_lo:[0,1] neg_hi:[0,1]
	v_pk_mul_f32 v[176:177], v[188:189], v[132:133] op_sel_hi:[0,1]
	v_pk_fma_f32 v[228:229], v[188:189], v[132:133], v[176:177] op_sel:[1,0,1] op_sel_hi:[1,1,0]
	v_pk_fma_f32 v[132:133], v[188:189], v[132:133], v[176:177] op_sel:[1,0,1] op_sel_hi:[1,1,0] neg_lo:[0,0,1] neg_hi:[0,0,1]
	v_cndmask_b32_e64 v177, v99, v193, s[44:45]
	v_cndmask_b32_e64 v176, v193, v192, s[44:45]
	v_pk_mul_f32 v[126:127], v[124:125], v[176:177] op_sel:[1,1] op_sel_hi:[1,0]
	v_mov_b32_e32 v229, v133
	v_pk_fma_f32 v[130:131], v[124:125], v[176:177], v[126:127] neg_lo:[0,0,1] neg_hi:[0,0,1]
	v_pk_fma_f32 v[124:125], v[124:125], v[176:177], v[126:127] op_sel_hi:[0,1,1]
	v_mov_b32_e32 v131, v125
	v_pk_fma_f32 v[124:125], v[116:117], v[188:189], v[120:121] neg_lo:[0,0,1] neg_hi:[0,0,1]
	v_pk_fma_f32 v[116:117], v[116:117], v[188:189], v[120:121] op_sel_hi:[0,1,1]
	v_mov_b32_e32 v125, v117
	v_pk_add_f32 v[116:117], v[118:119], v[122:123] neg_lo:[0,1] neg_hi:[0,1]
	v_pk_add_f32 v[132:133], v[208:209], v[228:229] neg_lo:[0,1] neg_hi:[0,1]
	v_pk_mul_f32 v[118:119], v[116:117], v[188:189] op_sel_hi:[1,0]
	v_mov_b32_e32 v99, s18
	v_pk_fma_f32 v[120:121], v[116:117], v[188:189], v[118:119] op_sel:[0,1,1] op_sel_hi:[1,1,0]
	v_pk_fma_f32 v[116:117], v[116:117], v[188:189], v[118:119] op_sel:[0,1,1] op_sel_hi:[1,1,0] neg_lo:[0,0,1] neg_hi:[0,0,1]
	s_nop 0
	v_mov_b32_e32 v121, v117
	v_pk_add_f32 v[118:119], v[124:125], v[120:121] neg_lo:[0,1] neg_hi:[0,1]
	v_pk_add_f32 v[116:117], v[124:125], v[120:121]
	v_pk_mul_f32 v[120:121], v[176:177], v[118:119] op_sel:[1,1] op_sel_hi:[0,1]
	v_pk_fma_f32 v[122:123], v[176:177], v[118:119], v[120:121] neg_lo:[0,0,1] neg_hi:[0,0,1]
	v_pk_fma_f32 v[118:119], v[176:177], v[118:119], v[120:121] op_sel_hi:[1,0,1]
	s_nop 0
	v_mov_b32_e32 v123, v119
	v_pk_fma_f32 v[118:119], v[100:101], v[184:185], v[108:109] neg_lo:[0,0,1] neg_hi:[0,0,1]
	v_pk_fma_f32 v[100:101], v[100:101], v[184:185], v[108:109] op_sel_hi:[0,1,1]
	v_mov_b32_e32 v119, v101
	v_pk_add_f32 v[100:101], v[104:105], v[112:113] neg_lo:[0,1] neg_hi:[0,1]
	s_nop 0
	v_pk_mul_f32 v[104:105], v[100:101], v[184:185] op_sel_hi:[1,0]
	s_nop 0
	v_pk_fma_f32 v[108:109], v[100:101], v[184:185], v[104:105] op_sel:[0,1,1] op_sel_hi:[1,1,0]
	v_pk_fma_f32 v[100:101], v[100:101], v[184:185], v[104:105] op_sel:[0,1,1] op_sel_hi:[1,1,0] neg_lo:[0,0,1] neg_hi:[0,0,1]
	v_pk_mul_f32 v[104:105], v[102:103], v[186:187] op_sel:[1,1] op_sel_hi:[1,0]
	v_mov_b32_e32 v109, v101
	v_pk_fma_f32 v[110:111], v[102:103], v[186:187], v[104:105] neg_lo:[0,0,1] neg_hi:[0,0,1]
	v_pk_fma_f32 v[102:103], v[102:103], v[186:187], v[104:105] op_sel_hi:[0,1,1]
	v_mov_b32_e32 v111, v103
	v_pk_add_f32 v[102:103], v[106:107], v[114:115] neg_lo:[0,1] neg_hi:[0,1]
	v_pk_add_f32 v[100:101], v[118:119], v[108:109]
	v_pk_mul_f32 v[104:105], v[102:103], v[190:191] op_sel_hi:[1,0]
	v_pk_add_f32 v[114:115], v[220:221], v[222:223]
	v_pk_fma_f32 v[106:107], v[102:103], v[190:191], v[104:105] op_sel:[0,1,1] op_sel_hi:[1,1,0]
	v_pk_fma_f32 v[102:103], v[102:103], v[190:191], v[104:105] op_sel:[0,1,1] op_sel_hi:[1,1,0] neg_lo:[0,0,1] neg_hi:[0,0,1]
	s_nop 0
	v_mov_b32_e32 v107, v103
	v_pk_add_f32 v[102:103], v[110:111], v[106:107]
	s_nop 0
	v_pk_add_f32 v[104:105], v[100:101], v[102:103]
	v_pk_add_f32 v[100:101], v[100:101], v[102:103] neg_lo:[0,1] neg_hi:[0,1]
	s_nop 0
	v_pk_mul_f32 v[102:103], v[176:177], v[100:101] op_sel:[1,1] op_sel_hi:[0,1]
	v_pk_fma_f32 v[112:113], v[176:177], v[100:101], v[102:103] neg_lo:[0,0,1] neg_hi:[0,0,1]
	v_pk_fma_f32 v[100:101], v[176:177], v[100:101], v[102:103] op_sel_hi:[1,0,1]
	s_nop 0
	v_mov_b32_e32 v113, v101
; template <int R, class XT, class TWT>
; __device__ __forceinline__ void dif_task(XT X, TWT tw, int s, int task) {
;     const int lgM = 13 - s, lgq = lgM - R, q = 1 << lgq;
;     const int j0 = task & (q - 1), blk = task >> lgq, base = (blk << lgM) + j0;
;     const int pb = PADI(base), qp = (q >= 32) ? q + (q >> 4) : q;
;     f32x2v v[1 << R];
; #pragma unroll
;     for (int k = 0; k < (1 << R); ++k) v[k] = X[pb + k * qp];
; #pragma unroll
;     for (int r = 0; r < R; ++r) {
;         const int pb = R - 1 - r;
; #pragma unroll
;         for (int k = 0; k < (1 << R); ++k) if (!((k >> pb) & 1)) {
;             const int klo = k & ((1 << pb) - 1);
;             const f32x2v w = tw[(j0 + (klo << lgq)) << (s + r)];
;             const f32x2v a = v[k], b = v[k + (1 << pb)], d = a - b;
;             v[k] = a + b; v[k + (1 << pb)] = (f32x2v){d.x * w.x - d.y * w.y, d.x * w.y + d.y * w.x};
;         }
;     }
; #pragma unroll
;     for (int k = 0; k < (1 << R); ++k) X[pb + k * qp] = v[k];
; }
	v_pk_add_f32 v[100:101], v[118:119], v[108:109] neg_lo:[0,1] neg_hi:[0,1]
	v_pk_add_f32 v[118:119], v[224:225], v[226:227]
	v_pk_mul_f32 v[102:103], v[188:189], v[100:101] op_sel:[1,1] op_sel_hi:[0,1]
	v_pk_fma_f32 v[108:109], v[188:189], v[100:101], v[102:103] neg_lo:[0,0,1] neg_hi:[0,0,1]
	v_pk_fma_f32 v[100:101], v[188:189], v[100:101], v[102:103] op_sel_hi:[1,0,1]
	v_pk_add_f32 v[120:121], v[114:115], v[118:119]
	v_mov_b32_e32 v109, v101
	v_pk_add_f32 v[100:101], v[110:111], v[106:107] neg_lo:[0,1] neg_hi:[0,1]
	s_nop 0
	v_pk_mul_f32 v[102:103], v[188:189], v[100:101] op_sel_hi:[0,1]
	v_pk_fma_f32 v[106:107], v[188:189], v[100:101], v[102:103] op_sel:[1,0,1] op_sel_hi:[1,1,0]
	v_pk_fma_f32 v[100:101], v[188:189], v[100:101], v[102:103] op_sel:[1,0,1] op_sel_hi:[1,1,0] neg_lo:[0,0,1] neg_hi:[0,0,1]
	s_nop 0
	v_mov_b32_e32 v107, v101
	v_pk_add_f32 v[102:103], v[108:109], v[106:107] neg_lo:[0,1] neg_hi:[0,1]
	v_pk_add_f32 v[100:101], v[108:109], v[106:107]
	v_pk_mul_f32 v[106:107], v[176:177], v[102:103] op_sel:[1,1] op_sel_hi:[0,1]
	v_pk_fma_f32 v[108:109], v[176:177], v[102:103], v[106:107] neg_lo:[0,0,1] neg_hi:[0,0,1]
	v_pk_fma_f32 v[102:103], v[176:177], v[102:103], v[106:107] op_sel_hi:[1,0,1]
	v_pk_add_f32 v[106:107], v[204:205], v[206:207]
	v_mov_b32_e32 v109, v103
	v_pk_add_f32 v[102:103], v[198:199], v[202:203]
	s_nop 0
	v_pk_add_f32 v[110:111], v[102:103], v[106:107]
	v_pk_add_f32 v[102:103], v[102:103], v[106:107] neg_lo:[0,1] neg_hi:[0,1]
	v_pk_add_f32 v[124:125], v[110:111], v[120:121]
	v_pk_add_f32 v[110:111], v[110:111], v[120:121] neg_lo:[0,1] neg_hi:[0,1]
	v_pk_mul_f32 v[106:107], v[188:189], v[102:103] op_sel:[1,1] op_sel_hi:[0,1]
	v_pk_mul_f32 v[120:121], v[110:111], v[176:177] op_sel:[1,1] op_sel_hi:[1,0]
	s_nop 0
	v_pk_fma_f32 v[126:127], v[110:111], v[176:177], v[120:121] neg_lo:[0,0,1] neg_hi:[0,0,1]
	v_pk_fma_f32 v[110:111], v[110:111], v[176:177], v[120:121] op_sel_hi:[0,1,1]
	v_mov_b32_e32 v127, v111
	v_pk_fma_f32 v[110:111], v[188:189], v[102:103], v[106:107] neg_lo:[0,0,1] neg_hi:[0,0,1]
	v_pk_fma_f32 v[102:103], v[188:189], v[102:103], v[106:107] op_sel_hi:[1,0,1]
	s_nop 0
	v_mov_b32_e32 v111, v103
	v_pk_add_f32 v[102:103], v[114:115], v[118:119] neg_lo:[0,1] neg_hi:[0,1]
	s_nop 0
	v_pk_mul_f32 v[106:107], v[188:189], v[102:103] op_sel_hi:[0,1]
	v_pk_fma_f32 v[114:115], v[188:189], v[102:103], v[106:107] op_sel:[1,0,1] op_sel_hi:[1,1,0]
	v_pk_fma_f32 v[102:103], v[188:189], v[102:103], v[106:107] op_sel:[1,0,1] op_sel_hi:[1,1,0] neg_lo:[0,0,1] neg_hi:[0,0,1]
	s_nop 0
	v_mov_b32_e32 v115, v103
	v_pk_add_f32 v[106:107], v[110:111], v[114:115] neg_lo:[0,1] neg_hi:[0,1]
	v_pk_add_f32 v[102:103], v[110:111], v[114:115]
	v_pk_mul_f32 v[110:111], v[176:177], v[106:107] op_sel:[1,1] op_sel_hi:[0,1]
	v_pk_fma_f32 v[114:115], v[176:177], v[106:107], v[110:111] neg_lo:[0,0,1] neg_hi:[0,0,1]
	v_pk_fma_f32 v[106:107], v[176:177], v[106:107], v[110:111] op_sel_hi:[1,0,1]
	v_pk_add_f32 v[110:111], v[178:179], v[182:183]
	v_mov_b32_e32 v115, v107
	v_pk_add_f32 v[106:107], v[196:197], v[194:195]
	s_nop 0
	v_pk_add_f32 v[118:119], v[106:107], v[110:111]
	v_pk_add_f32 v[106:107], v[106:107], v[110:111] neg_lo:[0,1] neg_hi:[0,1]
	s_nop 0
	v_pk_mul_f32 v[110:111], v[176:177], v[106:107] op_sel:[1,1] op_sel_hi:[0,1]
	v_pk_fma_f32 v[120:121], v[176:177], v[106:107], v[110:111] neg_lo:[0,0,1] neg_hi:[0,0,1]
	v_pk_fma_f32 v[106:107], v[176:177], v[106:107], v[110:111] op_sel_hi:[1,0,1]
	v_pk_mul_f32 v[110:111], v[176:177], v[132:133] op_sel:[1,1] op_sel_hi:[0,1]
	v_pk_fma_f32 v[178:179], v[176:177], v[132:133], v[110:111] neg_lo:[0,0,1] neg_hi:[0,0,1]
	v_pk_fma_f32 v[110:111], v[176:177], v[132:133], v[110:111] op_sel_hi:[1,0,1]
	v_mov_b32_e32 v121, v107
	v_pk_add_f32 v[106:107], v[208:209], v[228:229]
	v_mov_b32_e32 v179, v111
	ds_write2_b64 v135, v[128:129], v[130:131] offset1:34
	ds_write2_b64 v135, v[116:117], v[122:123] offset0:68 offset1:102
	ds_write2_b64 v135, v[104:105], v[112:113] offset0:136 offset1:170
	ds_write2_b64 v135, v[100:101], v[108:109] offset0:204 offset1:238
	ds_write2_b64 v98, v[124:125], v[126:127] offset0:16 offset1:50
	ds_write2_b64 v98, v[102:103], v[114:115] offset0:84 offset1:118
	ds_write2_b64 v98, v[118:119], v[120:121] offset0:152 offset1:186
	ds_write2_b64 v98, v[106:107], v[178:179] offset0:220 offset1:254
	s_waitcnt lgkmcnt(0)
	s_barrier
; #define LAS __attribute__((address_space(3)))
; __device__ __forceinline__ void lds_barrier() { asm volatile("s_waitcnt lgkmcnt(0)" ::: "memory"); __builtin_amdgcn_s_barrier(); asm volatile("" ::: "memory"); }
; template <int R, class XT, class TWT>
; __device__ __forceinline__ void dif_task(XT X, TWT tw, int s, int task) {
;     const int lgM = 13 - s, lgq = lgM - R, q = 1 << lgq;
;     const int j0 = task & (q - 1), blk = task >> lgq, base = (blk << lgM) + j0;
;     const int pb = PADI(base), qp = (q >= 32) ? q + (q >> 4) : q;
;     f32x2v v[1 << R];
; #pragma unroll
;     for (int k = 0; k < (1 << R); ++k) v[k] = X[pb + k * qp];
; #pragma unroll
;     for (int r = 0; r < R; ++r) {
;         const int pb = R - 1 - r;
; #pragma unroll
;         for (int k = 0; k < (1 << R); ++k) if (!((k >> pb) & 1)) {
;             const int klo = k & ((1 << pb) - 1);
;             const f32x2v w = tw[(j0 + (klo << lgq)) << (s + r)];
;             const f32x2v a = v[k], b = v[k + (1 << pb)], d = a - b;
;             v[k] = a + b; v[k + (1 << pb)] = (f32x2v){d.x * w.x - d.y * w.y, d.x * w.y + d.y * w.x};
;         }
;     }
; #pragma unroll
;     for (int k = 0; k < (1 << R); ++k) X[pb + k * qp] = v[k];
; }
; __device__ __forceinline__ void fft_fwd_upper(LAS f32x2v* X, TwHalf tw, int s0, int tid) {
;     if (s0 == 0) { dif_task<4>(X, tw, 0, tid); lds_barrier(); }
;     dif_task<4>(X, tw, 4, tid); lds_barrier();
;     dif_task<4>(X, tw, 8, tid); lds_barrier();
; }
	ds_read2_b64 v[100:103], v137 offset1:2
	ds_read2_b64 v[104:107], v137 offset0:4 offset1:6
	ds_read2_b64 v[108:111], v137 offset0:8 offset1:10
	ds_read2_b64 v[112:115], v137 offset0:12 offset1:14
	ds_read2_b64 v[116:119], v137 offset0:16 offset1:18
	ds_read2_b64 v[120:123], v137 offset0:20 offset1:22
	ds_read2_b64 v[124:127], v137 offset0:24 offset1:26
	ds_read2_b64 v[128:131], v137 offset0:28 offset1:30
	ds_read2st64_b64 v[176:179], v170 offset1:16
	ds_read_b64 v[132:133], v171
	ds_read_b64 v[182:183], v172
	ds_read_b64 v[184:185], v173
	ds_read_b64 v[186:187], v156
	s_waitcnt lgkmcnt(8)
	v_pk_add_f32 v[194:195], v[100:101], v[116:117] neg_lo:[0,1] neg_hi:[0,1]
	ds_read_b64 v[188:189], v174
	ds_read_b64 v[190:191], v175
	ds_read_b64 v[192:193], v99
	s_waitcnt lgkmcnt(7)
	v_pk_mul_f32 v[196:197], v[194:195], v[176:177] op_sel:[1,1] op_sel_hi:[1,0]
	v_pk_add_f32 v[100:101], v[100:101], v[116:117]
	v_pk_fma_f32 v[198:199], v[194:195], v[176:177], v[196:197] neg_lo:[0,0,1] neg_hi:[0,0,1]
	v_pk_fma_f32 v[194:195], v[194:195], v[176:177], v[196:197] op_sel_hi:[0,1,1]
	v_mov_b32_e32 v199, v195
	v_pk_add_f32 v[194:195], v[108:109], v[124:125] neg_lo:[0,1] neg_hi:[0,1]
	v_pk_add_f32 v[108:109], v[108:109], v[124:125]
	v_pk_mul_f32 v[196:197], v[194:195], v[176:177] op_sel:[1,0] op_sel_hi:[0,0]
	v_pk_fma_f32 v[202:203], v[194:195], v[176:177], v[196:197] op_sel:[0,1,0]
	v_pk_fma_f32 v[176:177], v[194:195], v[176:177], v[196:197] op_sel:[0,1,0] neg_lo:[0,0,1] neg_hi:[0,0,1]
	v_pk_add_f32 v[116:117], v[100:101], v[108:109]
	v_mov_b32_e32 v203, v177
	v_pk_add_f32 v[176:177], v[198:199], v[202:203] neg_lo:[0,1] neg_hi:[0,1]
	v_pk_add_f32 v[100:101], v[100:101], v[108:109] neg_lo:[0,1] neg_hi:[0,1]
	s_waitcnt lgkmcnt(4)
	v_pk_mul_f32 v[194:195], v[184:185], v[176:177] op_sel:[1,1] op_sel_hi:[0,1]
	v_pk_fma_f32 v[196:197], v[184:185], v[176:177], v[194:195] neg_lo:[0,0,1] neg_hi:[0,0,1]
	v_pk_fma_f32 v[176:177], v[184:185], v[176:177], v[194:195] op_sel_hi:[1,0,1]
	v_pk_mul_f32 v[108:109], v[100:101], v[184:185] op_sel:[1,1] op_sel_hi:[1,0]
	v_mov_b32_e32 v197, v177
	v_pk_add_f32 v[176:177], v[104:105], v[120:121] neg_lo:[0,1] neg_hi:[0,1]
	v_pk_add_f32 v[104:105], v[104:105], v[120:121]
	v_pk_mul_f32 v[194:195], v[176:177], v[178:179] op_sel:[1,1] op_sel_hi:[1,0]
	s_nop 0
	v_pk_fma_f32 v[204:205], v[176:177], v[178:179], v[194:195] neg_lo:[0,0,1] neg_hi:[0,0,1]
	v_pk_fma_f32 v[176:177], v[176:177], v[178:179], v[194:195] op_sel_hi:[0,1,1]
	v_mov_b32_e32 v205, v177
	v_pk_add_f32 v[176:177], v[112:113], v[128:129] neg_lo:[0,1] neg_hi:[0,1]
	v_pk_add_f32 v[112:113], v[112:113], v[128:129]
	v_pk_mul_f32 v[194:195], v[176:177], v[178:179] op_sel:[1,0] op_sel_hi:[0,0]
	v_pk_fma_f32 v[206:207], v[176:177], v[178:179], v[194:195] op_sel:[0,1,0]
	v_pk_fma_f32 v[176:177], v[176:177], v[178:179], v[194:195] op_sel:[0,1,0] neg_lo:[0,0,1] neg_hi:[0,0,1]
	v_pk_add_f32 v[120:121], v[104:105], v[112:113]
	v_mov_b32_e32 v207, v177
	v_pk_add_f32 v[176:177], v[204:205], v[206:207] neg_lo:[0,1] neg_hi:[0,1]
	v_pk_add_f32 v[124:125], v[116:117], v[120:121]
	v_pk_mul_f32 v[178:179], v[184:185], v[176:177] op_sel_hi:[0,1]
	v_pk_fma_f32 v[194:195], v[184:185], v[176:177], v[178:179] op_sel:[1,0,1] op_sel_hi:[1,1,0]
	v_pk_fma_f32 v[176:177], v[184:185], v[176:177], v[178:179] op_sel:[1,0,1] op_sel_hi:[1,1,0] neg_lo:[0,0,1] neg_hi:[0,0,1]
	v_pk_add_f32 v[116:117], v[116:117], v[120:121] neg_lo:[0,1] neg_hi:[0,1]
	v_mov_b32_e32 v195, v177
	v_pk_add_f32 v[176:177], v[196:197], v[194:195] neg_lo:[0,1] neg_hi:[0,1]
	s_waitcnt lgkmcnt(1)
	v_pk_mul_f32 v[120:121], v[116:117], v[190:191] op_sel:[1,1] op_sel_hi:[1,0]
	v_pk_mul_f32 v[178:179], v[190:191], v[176:177] op_sel:[1,1] op_sel_hi:[0,1]
	v_pk_fma_f32 v[208:209], v[190:191], v[176:177], v[178:179] neg_lo:[0,0,1] neg_hi:[0,0,1]
	v_pk_fma_f32 v[176:177], v[190:191], v[176:177], v[178:179] op_sel_hi:[1,0,1]
	s_nop 0
	v_mov_b32_e32 v209, v177
	v_pk_add_f32 v[176:177], v[102:103], v[118:119] neg_lo:[0,1] neg_hi:[0,1]
	v_pk_add_f32 v[102:103], v[102:103], v[118:119]
	v_pk_mul_f32 v[178:179], v[176:177], v[132:133] op_sel:[1,1] op_sel_hi:[1,0]
	s_nop 0
	v_pk_fma_f32 v[220:221], v[176:177], v[132:133], v[178:179] neg_lo:[0,0,1] neg_hi:[0,0,1]
	v_pk_fma_f32 v[176:177], v[176:177], v[132:133], v[178:179] op_sel_hi:[0,1,1]
	v_mov_b32_e32 v221, v177
	v_pk_add_f32 v[176:177], v[110:111], v[126:127] neg_lo:[0,1] neg_hi:[0,1]
	v_pk_add_f32 v[110:111], v[110:111], v[126:127]
	v_pk_mul_f32 v[178:179], v[176:177], v[132:133] op_sel:[1,0] op_sel_hi:[0,0]
	v_pk_fma_f32 v[222:223], v[176:177], v[132:133], v[178:179] op_sel:[0,1,0]
	v_pk_fma_f32 v[132:133], v[176:177], v[132:133], v[178:179] op_sel:[0,1,0] neg_lo:[0,0,1] neg_hi:[0,0,1]
	v_pk_add_f32 v[118:119], v[102:103], v[110:111]
	v_mov_b32_e32 v223, v133
	v_pk_add_f32 v[132:133], v[220:221], v[222:223] neg_lo:[0,1] neg_hi:[0,1]
	v_pk_add_f32 v[102:103], v[102:103], v[110:111] neg_lo:[0,1] neg_hi:[0,1]
	v_pk_mul_f32 v[176:177], v[188:189], v[132:133] op_sel:[1,1] op_sel_hi:[0,1]
	v_pk_fma_f32 v[178:179], v[188:189], v[132:133], v[176:177] neg_lo:[0,0,1] neg_hi:[0,0,1]
	v_pk_fma_f32 v[132:133], v[188:189], v[132:133], v[176:177] op_sel_hi:[1,0,1]
	s_nop 0
	v_mov_b32_e32 v179, v133
	v_pk_add_f32 v[132:133], v[106:107], v[122:123] neg_lo:[0,1] neg_hi:[0,1]
	v_pk_add_f32 v[106:107], v[106:107], v[122:123]
	v_pk_mul_f32 v[176:177], v[132:133], v[182:183] op_sel:[1,1] op_sel_hi:[1,0]
	s_nop 0
	v_pk_fma_f32 v[224:225], v[132:133], v[182:183], v[176:177] neg_lo:[0,0,1] neg_hi:[0,0,1]
	v_pk_fma_f32 v[132:133], v[132:133], v[182:183], v[176:177] op_sel_hi:[0,1,1]
	v_mov_b32_e32 v225, v133
	v_pk_add_f32 v[132:133], v[114:115], v[130:131] neg_lo:[0,1] neg_hi:[0,1]
	v_pk_add_f32 v[114:115], v[114:115], v[130:131]
	v_pk_mul_f32 v[176:177], v[132:133], v[182:183] op_sel:[1,0] op_sel_hi:[0,0]
	v_pk_fma_f32 v[226:227], v[132:133], v[182:183], v[176:177] op_sel:[0,1,0]
	v_pk_fma_f32 v[132:133], v[132:133], v[182:183], v[176:177] op_sel:[0,1,0] neg_lo:[0,0,1] neg_hi:[0,0,1]
	v_pk_add_f32 v[122:123], v[106:107], v[114:115]
	v_mov_b32_e32 v227, v133
	v_pk_add_f32 v[132:133], v[224:225], v[226:227] neg_lo:[0,1] neg_hi:[0,1]
	v_pk_add_f32 v[126:127], v[118:119], v[122:123]
	v_pk_mul_f32 v[176:177], v[186:187], v[132:133] op_sel_hi:[0,1]
	v_pk_fma_f32 v[182:183], v[186:187], v[132:133], v[176:177] op_sel:[1,0,1] op_sel_hi:[1,1,0]
	v_pk_fma_f32 v[132:133], v[186:187], v[132:133], v[176:177] op_sel:[1,0,1] op_sel_hi:[1,1,0] neg_lo:[0,0,1] neg_hi:[0,0,1]
	v_pk_add_f32 v[128:129], v[124:125], v[126:127]
	v_mov_b32_e32 v183, v133
	v_pk_add_f32 v[132:133], v[178:179], v[182:183] neg_lo:[0,1] neg_hi:[0,1]
	v_pk_add_f32 v[124:125], v[124:125], v[126:127] neg_lo:[0,1] neg_hi:[0,1]
	v_pk_mul_f32 v[176:177], v[190:191], v[132:133] op_sel_hi:[0,1]
	v_pk_fma_f32 v[228:229], v[190:191], v[132:133], v[176:177] op_sel:[1,0,1] op_sel_hi:[1,1,0]
	v_pk_fma_f32 v[132:133], v[190:191], v[132:133], v[176:177] op_sel:[1,0,1] op_sel_hi:[1,1,0] neg_lo:[0,0,1] neg_hi:[0,0,1]
	s_waitcnt lgkmcnt(0)
; template <int R, class XT, class TWT>
; __device__ __forceinline__ void dif_task(XT X, TWT tw, int s, int task) {
;     const int lgM = 13 - s, lgq = lgM - R, q = 1 << lgq;
;     const int j0 = task & (q - 1), blk = task >> lgq, base = (blk << lgM) + j0;
;     const int pb = PADI(base), qp = (q >= 32) ? q + (q >> 4) : q;
;     f32x2v v[1 << R];
; #pragma unroll
;     for (int k = 0; k < (1 << R); ++k) v[k] = X[pb + k * qp];
; #pragma unroll
;     for (int r = 0; r < R; ++r) {
;         const int pb = R - 1 - r;
; #pragma unroll
;         for (int k = 0; k < (1 << R); ++k) if (!((k >> pb) & 1)) {
;             const int klo = k & ((1 << pb) - 1);
;             const f32x2v w = tw[(j0 + (klo << lgq)) << (s + r)];
;             const f32x2v a = v[k], b = v[k + (1 << pb)], d = a - b;
;             v[k] = a + b; v[k + (1 << pb)] = (f32x2v){d.x * w.x - d.y * w.y, d.x * w.y + d.y * w.x};
;         }
;     }
; #pragma unroll
;     for (int k = 0; k < (1 << R); ++k) X[pb + k * qp] = v[k];
; }
	v_xor_b32_e32 v176, 0x80000000, v192
	v_cndmask_b32_e64 v177, v176, v193, s[42:43]
	v_cndmask_b32_e64 v176, v193, v192, s[42:43]
	v_pk_mul_f32 v[126:127], v[124:125], v[176:177] op_sel:[1,1] op_sel_hi:[1,0]
	v_mov_b32_e32 v229, v133
	v_pk_fma_f32 v[130:131], v[124:125], v[176:177], v[126:127] neg_lo:[0,0,1] neg_hi:[0,0,1]
	v_pk_fma_f32 v[124:125], v[124:125], v[176:177], v[126:127] op_sel_hi:[0,1,1]
	v_mov_b32_e32 v131, v125
	v_pk_fma_f32 v[124:125], v[116:117], v[190:191], v[120:121] neg_lo:[0,0,1] neg_hi:[0,0,1]
	v_pk_fma_f32 v[116:117], v[116:117], v[190:191], v[120:121] op_sel_hi:[0,1,1]
	v_mov_b32_e32 v125, v117
	v_pk_add_f32 v[116:117], v[118:119], v[122:123] neg_lo:[0,1] neg_hi:[0,1]
	v_pk_add_f32 v[132:133], v[208:209], v[228:229] neg_lo:[0,1] neg_hi:[0,1]
	v_pk_mul_f32 v[118:119], v[116:117], v[190:191] op_sel_hi:[1,0]
	s_nop 0
	v_pk_fma_f32 v[120:121], v[116:117], v[190:191], v[118:119] op_sel:[0,1,1] op_sel_hi:[1,1,0]
	v_pk_fma_f32 v[116:117], v[116:117], v[190:191], v[118:119] op_sel:[0,1,1] op_sel_hi:[1,1,0] neg_lo:[0,0,1] neg_hi:[0,0,1]
	s_nop 0
	v_mov_b32_e32 v121, v117
	v_pk_add_f32 v[118:119], v[124:125], v[120:121] neg_lo:[0,1] neg_hi:[0,1]
	v_pk_add_f32 v[116:117], v[124:125], v[120:121]
	v_pk_mul_f32 v[120:121], v[176:177], v[118:119] op_sel:[1,1] op_sel_hi:[0,1]
	v_pk_fma_f32 v[122:123], v[176:177], v[118:119], v[120:121] neg_lo:[0,0,1] neg_hi:[0,0,1]
	v_pk_fma_f32 v[118:119], v[176:177], v[118:119], v[120:121] op_sel_hi:[1,0,1]
	s_nop 0
	v_mov_b32_e32 v123, v119
	v_pk_fma_f32 v[118:119], v[100:101], v[184:185], v[108:109] neg_lo:[0,0,1] neg_hi:[0,0,1]
	v_pk_fma_f32 v[100:101], v[100:101], v[184:185], v[108:109] op_sel_hi:[0,1,1]
	v_mov_b32_e32 v119, v101
	v_pk_add_f32 v[100:101], v[104:105], v[112:113] neg_lo:[0,1] neg_hi:[0,1]
	s_nop 0
	v_pk_mul_f32 v[104:105], v[100:101], v[184:185] op_sel_hi:[1,0]
	s_nop 0
	v_pk_fma_f32 v[108:109], v[100:101], v[184:185], v[104:105] op_sel:[0,1,1] op_sel_hi:[1,1,0]
	v_pk_fma_f32 v[100:101], v[100:101], v[184:185], v[104:105] op_sel:[0,1,1] op_sel_hi:[1,1,0] neg_lo:[0,0,1] neg_hi:[0,0,1]
	v_pk_mul_f32 v[104:105], v[102:103], v[188:189] op_sel:[1,1] op_sel_hi:[1,0]
	v_mov_b32_e32 v109, v101
	v_pk_fma_f32 v[110:111], v[102:103], v[188:189], v[104:105] neg_lo:[0,0,1] neg_hi:[0,0,1]
	v_pk_fma_f32 v[102:103], v[102:103], v[188:189], v[104:105] op_sel_hi:[0,1,1]
	v_mov_b32_e32 v111, v103
	v_pk_add_f32 v[102:103], v[106:107], v[114:115] neg_lo:[0,1] neg_hi:[0,1]
	v_pk_add_f32 v[100:101], v[118:119], v[108:109]
	v_pk_mul_f32 v[104:105], v[102:103], v[186:187] op_sel_hi:[1,0]
	v_pk_add_f32 v[114:115], v[220:221], v[222:223]
	v_pk_fma_f32 v[106:107], v[102:103], v[186:187], v[104:105] op_sel:[0,1,1] op_sel_hi:[1,1,0]
	v_pk_fma_f32 v[102:103], v[102:103], v[186:187], v[104:105] op_sel:[0,1,1] op_sel_hi:[1,1,0] neg_lo:[0,0,1] neg_hi:[0,0,1]
	s_nop 0
	v_mov_b32_e32 v107, v103
	v_pk_add_f32 v[102:103], v[110:111], v[106:107]
	s_nop 0
	v_pk_add_f32 v[104:105], v[100:101], v[102:103]
	v_pk_add_f32 v[100:101], v[100:101], v[102:103] neg_lo:[0,1] neg_hi:[0,1]
	s_nop 0
	v_pk_mul_f32 v[102:103], v[176:177], v[100:101] op_sel:[1,1] op_sel_hi:[0,1]
	v_pk_fma_f32 v[112:113], v[176:177], v[100:101], v[102:103] neg_lo:[0,0,1] neg_hi:[0,0,1]
	v_pk_fma_f32 v[100:101], v[176:177], v[100:101], v[102:103] op_sel_hi:[1,0,1]
	s_nop 0
	v_mov_b32_e32 v113, v101
	v_pk_add_f32 v[100:101], v[118:119], v[108:109] neg_lo:[0,1] neg_hi:[0,1]
	v_pk_add_f32 v[118:119], v[224:225], v[226:227]
	v_pk_mul_f32 v[102:103], v[190:191], v[100:101] op_sel:[1,1] op_sel_hi:[0,1]
	v_pk_fma_f32 v[108:109], v[190:191], v[100:101], v[102:103] neg_lo:[0,0,1] neg_hi:[0,0,1]
	v_pk_fma_f32 v[100:101], v[190:191], v[100:101], v[102:103] op_sel_hi:[1,0,1]
	v_pk_add_f32 v[120:121], v[114:115], v[118:119]
	v_mov_b32_e32 v109, v101
	v_pk_add_f32 v[100:101], v[110:111], v[106:107] neg_lo:[0,1] neg_hi:[0,1]
	s_nop 0
	v_pk_mul_f32 v[102:103], v[190:191], v[100:101] op_sel_hi:[0,1]
	v_pk_fma_f32 v[106:107], v[190:191], v[100:101], v[102:103] op_sel:[1,0,1] op_sel_hi:[1,1,0]
	v_pk_fma_f32 v[100:101], v[190:191], v[100:101], v[102:103] op_sel:[1,0,1] op_sel_hi:[1,1,0] neg_lo:[0,0,1] neg_hi:[0,0,1]
	s_nop 0
	v_mov_b32_e32 v107, v101
	v_pk_add_f32 v[102:103], v[108:109], v[106:107] neg_lo:[0,1] neg_hi:[0,1]
	v_pk_add_f32 v[100:101], v[108:109], v[106:107]
	v_pk_mul_f32 v[106:107], v[176:177], v[102:103] op_sel:[1,1] op_sel_hi:[0,1]
	v_pk_fma_f32 v[108:109], v[176:177], v[102:103], v[106:107] neg_lo:[0,0,1] neg_hi:[0,0,1]
	v_pk_fma_f32 v[102:103], v[176:177], v[102:103], v[106:107] op_sel_hi:[1,0,1]
	v_pk_add_f32 v[106:107], v[204:205], v[206:207]
	v_mov_b32_e32 v109, v103
	v_pk_add_f32 v[102:103], v[198:199], v[202:203]
	s_nop 0
	v_pk_add_f32 v[110:111], v[102:103], v[106:107]
	v_pk_add_f32 v[102:103], v[102:103], v[106:107] neg_lo:[0,1] neg_hi:[0,1]
	v_pk_add_f32 v[124:125], v[110:111], v[120:121]
	v_pk_add_f32 v[110:111], v[110:111], v[120:121] neg_lo:[0,1] neg_hi:[0,1]
	v_pk_mul_f32 v[106:107], v[190:191], v[102:103] op_sel:[1,1] op_sel_hi:[0,1]
	v_pk_mul_f32 v[120:121], v[110:111], v[176:177] op_sel:[1,1] op_sel_hi:[1,0]
	s_nop 0
	v_pk_fma_f32 v[126:127], v[110:111], v[176:177], v[120:121] neg_lo:[0,0,1] neg_hi:[0,0,1]
	v_pk_fma_f32 v[110:111], v[110:111], v[176:177], v[120:121] op_sel_hi:[0,1,1]
	v_mov_b32_e32 v127, v111
	v_pk_fma_f32 v[110:111], v[190:191], v[102:103], v[106:107] neg_lo:[0,0,1] neg_hi:[0,0,1]
	v_pk_fma_f32 v[102:103], v[190:191], v[102:103], v[106:107] op_sel_hi:[1,0,1]
	s_nop 0
	v_mov_b32_e32 v111, v103
	v_pk_add_f32 v[102:103], v[114:115], v[118:119] neg_lo:[0,1] neg_hi:[0,1]
	s_nop 0
	v_pk_mul_f32 v[106:107], v[190:191], v[102:103] op_sel_hi:[0,1]
; __device__ __forceinline__ void lds_barrier() { asm volatile("s_waitcnt lgkmcnt(0)" ::: "memory"); __builtin_amdgcn_s_barrier(); asm volatile("" ::: "memory"); }
; template <int R, class XT, class TWT>
; __device__ __forceinline__ void dif_task(XT X, TWT tw, int s, int task) {
;     const int lgM = 13 - s, lgq = lgM - R, q = 1 << lgq;
;     const int j0 = task & (q - 1), blk = task >> lgq, base = (blk << lgM) + j0;
;     const int pb = PADI(base), qp = (q >= 32) ? q + (q >> 4) : q;
;     f32x2v v[1 << R];
; #pragma unroll
;     for (int k = 0; k < (1 << R); ++k) v[k] = X[pb + k * qp];
; #pragma unroll
;     for (int r = 0; r < R; ++r) {
;         const int pb = R - 1 - r;
; #pragma unroll
;         for (int k = 0; k < (1 << R); ++k) if (!((k >> pb) & 1)) {
;             const int klo = k & ((1 << pb) - 1);
;             const f32x2v w = tw[(j0 + (klo << lgq)) << (s + r)];
;             const f32x2v a = v[k], b = v[k + (1 << pb)], d = a - b;
;             v[k] = a + b; v[k + (1 << pb)] = (f32x2v){d.x * w.x - d.y * w.y, d.x * w.y + d.y * w.x};
;         }
;     }
; #pragma unroll
;     for (int k = 0; k < (1 << R); ++k) X[pb + k * qp] = v[k];
; }
; template <bool LAT>
; __device__ __forceinline__ void hyconv_unit(const Frame& F, LAS f32x2v* X, const TwHalf tw, LAS bf16* OUT, const float* skip, bf16* MIX, int u) {
;     ...
;             for (int r = 0; r < 8; ++r) { const int e = 2 * (F.tid + 512 * r);
;                 const f32x2v a = X[PADI(e)], b = X[PADI(e + 1)]; const f32x4 k = kq[r];
;                 const f32x2v p = a + b, q = a - b; const f32x2v pk = (f32x2v){p.x * k.x - p.y * k.y, p.x * k.y + p.y * k.x}, qk = (f32x2v){q.x * k.z - q.y * k.w, q.x * k.w + q.y * k.z};
;                 X[PADI(e)] = pk + qk; X[PADI(e + 1)] = pk - qk; }
;             lds_barrier();
	v_pk_fma_f32 v[114:115], v[190:191], v[102:103], v[106:107] op_sel:[1,0,1] op_sel_hi:[1,1,0]
	v_pk_fma_f32 v[102:103], v[190:191], v[102:103], v[106:107] op_sel:[1,0,1] op_sel_hi:[1,1,0] neg_lo:[0,0,1] neg_hi:[0,0,1]
	s_nop 0
	v_mov_b32_e32 v115, v103
	v_pk_add_f32 v[106:107], v[110:111], v[114:115] neg_lo:[0,1] neg_hi:[0,1]
	v_pk_add_f32 v[102:103], v[110:111], v[114:115]
	v_pk_mul_f32 v[110:111], v[176:177], v[106:107] op_sel:[1,1] op_sel_hi:[0,1]
	v_pk_fma_f32 v[114:115], v[176:177], v[106:107], v[110:111] neg_lo:[0,0,1] neg_hi:[0,0,1]
	v_pk_fma_f32 v[106:107], v[176:177], v[106:107], v[110:111] op_sel_hi:[1,0,1]
	v_pk_add_f32 v[110:111], v[178:179], v[182:183]
	v_mov_b32_e32 v115, v107
	v_pk_add_f32 v[106:107], v[196:197], v[194:195]
	s_nop 0
	v_pk_add_f32 v[118:119], v[106:107], v[110:111]
	v_pk_add_f32 v[106:107], v[106:107], v[110:111] neg_lo:[0,1] neg_hi:[0,1]
	s_nop 0
	v_pk_mul_f32 v[110:111], v[176:177], v[106:107] op_sel:[1,1] op_sel_hi:[0,1]
	v_pk_fma_f32 v[120:121], v[176:177], v[106:107], v[110:111] neg_lo:[0,0,1] neg_hi:[0,0,1]
	v_pk_fma_f32 v[106:107], v[176:177], v[106:107], v[110:111] op_sel_hi:[1,0,1]
	v_pk_mul_f32 v[110:111], v[176:177], v[132:133] op_sel:[1,1] op_sel_hi:[0,1]
	v_pk_fma_f32 v[178:179], v[176:177], v[132:133], v[110:111] neg_lo:[0,0,1] neg_hi:[0,0,1]
	v_pk_fma_f32 v[110:111], v[176:177], v[132:133], v[110:111] op_sel_hi:[1,0,1]
	v_mov_b32_e32 v121, v107
	v_pk_add_f32 v[106:107], v[208:209], v[228:229]
	v_mov_b32_e32 v179, v111
	ds_write2_b64 v137, v[128:129], v[130:131] offset1:2
	ds_write2_b64 v137, v[116:117], v[122:123] offset0:4 offset1:6
	ds_write2_b64 v137, v[104:105], v[112:113] offset0:8 offset1:10
	ds_write2_b64 v137, v[100:101], v[108:109] offset0:12 offset1:14
	ds_write2_b64 v137, v[124:125], v[126:127] offset0:16 offset1:18
	ds_write2_b64 v137, v[102:103], v[114:115] offset0:20 offset1:22
	ds_write2_b64 v137, v[118:119], v[120:121] offset0:24 offset1:26
	ds_write2_b64 v137, v[106:107], v[178:179] offset0:28 offset1:30
	s_waitcnt lgkmcnt(0)
	s_barrier
	ds_read_b128 v[100:103], v157
	s_waitcnt lgkmcnt(0)
	v_pk_add_f32 v[104:105], v[100:101], v[102:103]
	v_pk_add_f32 v[100:101], v[100:101], v[102:103] neg_lo:[0,1] neg_hi:[0,1]
	s_waitcnt vmcnt(7)
	v_pk_mul_f32 v[102:103], v[28:29], v[104:105] op_sel:[1,1] op_sel_hi:[0,1]
	v_pk_fma_f32 v[106:107], v[28:29], v[104:105], v[102:103] neg_lo:[0,0,1] neg_hi:[0,0,1]
	v_pk_fma_f32 v[28:29], v[28:29], v[104:105], v[102:103] op_sel_hi:[1,0,1]
	s_nop 0
	v_mov_b32_e32 v107, v29
	v_pk_mul_f32 v[28:29], v[30:31], v[100:101] op_sel:[1,1] op_sel_hi:[0,1]
	v_pk_fma_f32 v[102:103], v[30:31], v[100:101], v[28:29] neg_lo:[0,0,1] neg_hi:[0,0,1]
	v_pk_fma_f32 v[28:29], v[30:31], v[100:101], v[28:29] op_sel_hi:[1,0,1]
	s_nop 0
	v_mov_b32_e32 v103, v29
	v_pk_add_f32 v[28:29], v[106:107], v[102:103]
	v_pk_add_f32 v[30:31], v[106:107], v[102:103] neg_lo:[0,1] neg_hi:[0,1]
	ds_write_b128 v157, v[28:31]
	ds_read_b128 v[28:31], v158 offset:8192
	s_waitcnt lgkmcnt(0)
	v_pk_add_f32 v[100:101], v[28:29], v[30:31]
	v_pk_add_f32 v[28:29], v[28:29], v[30:31] neg_lo:[0,1] neg_hi:[0,1]
	s_waitcnt vmcnt(6)
	v_pk_mul_f32 v[30:31], v[24:25], v[100:101] op_sel:[1,1] op_sel_hi:[0,1]
	v_pk_fma_f32 v[102:103], v[24:25], v[100:101], v[30:31] neg_lo:[0,0,1] neg_hi:[0,0,1]
	v_pk_fma_f32 v[24:25], v[24:25], v[100:101], v[30:31] op_sel_hi:[1,0,1]
	s_nop 0
	v_mov_b32_e32 v103, v25
	v_pk_mul_f32 v[24:25], v[26:27], v[28:29] op_sel:[1,1] op_sel_hi:[0,1]
	v_pk_fma_f32 v[30:31], v[26:27], v[28:29], v[24:25] neg_lo:[0,0,1] neg_hi:[0,0,1]
	v_pk_fma_f32 v[24:25], v[26:27], v[28:29], v[24:25] op_sel_hi:[1,0,1]
	s_nop 0
	v_mov_b32_e32 v31, v25
	v_pk_add_f32 v[24:25], v[102:103], v[30:31]
	v_pk_add_f32 v[26:27], v[102:103], v[30:31] neg_lo:[0,1] neg_hi:[0,1]
	ds_write_b128 v158, v[24:27] offset:8192
	ds_read_b128 v[24:27], v159 offset:16384
	s_waitcnt lgkmcnt(0)
	v_pk_add_f32 v[28:29], v[24:25], v[26:27]
	v_pk_add_f32 v[24:25], v[24:25], v[26:27] neg_lo:[0,1] neg_hi:[0,1]
	s_waitcnt vmcnt(5)
	v_pk_mul_f32 v[26:27], v[20:21], v[28:29] op_sel:[1,1] op_sel_hi:[0,1]
	v_pk_fma_f32 v[30:31], v[20:21], v[28:29], v[26:27] neg_lo:[0,0,1] neg_hi:[0,0,1]
	v_pk_fma_f32 v[20:21], v[20:21], v[28:29], v[26:27] op_sel_hi:[1,0,1]
	s_nop 0
	v_mov_b32_e32 v31, v21
	v_pk_mul_f32 v[20:21], v[22:23], v[24:25] op_sel:[1,1] op_sel_hi:[0,1]
	v_pk_fma_f32 v[26:27], v[22:23], v[24:25], v[20:21] neg_lo:[0,0,1] neg_hi:[0,0,1]
	v_pk_fma_f32 v[20:21], v[22:23], v[24:25], v[20:21] op_sel_hi:[1,0,1]
	s_nop 0
	v_mov_b32_e32 v27, v21
	v_pk_add_f32 v[20:21], v[30:31], v[26:27]
	v_pk_add_f32 v[22:23], v[30:31], v[26:27] neg_lo:[0,1] neg_hi:[0,1]
	ds_write_b128 v159, v[20:23] offset:16384
	ds_read_b128 v[20:23], v160 offset:24576
	s_waitcnt lgkmcnt(0)
	v_pk_add_f32 v[24:25], v[20:21], v[22:23]
	v_pk_add_f32 v[20:21], v[20:21], v[22:23] neg_lo:[0,1] neg_hi:[0,1]
	s_waitcnt vmcnt(4)
	v_pk_mul_f32 v[22:23], v[16:17], v[24:25] op_sel:[1,1] op_sel_hi:[0,1]
	v_pk_fma_f32 v[26:27], v[16:17], v[24:25], v[22:23] neg_lo:[0,0,1] neg_hi:[0,0,1]
	v_pk_fma_f32 v[16:17], v[16:17], v[24:25], v[22:23] op_sel_hi:[1,0,1]
	s_nop 0
	v_mov_b32_e32 v27, v17
	v_pk_mul_f32 v[16:17], v[18:19], v[20:21] op_sel:[1,1] op_sel_hi:[0,1]
	v_pk_fma_f32 v[22:23], v[18:19], v[20:21], v[16:17] neg_lo:[0,0,1] neg_hi:[0,0,1]
	v_pk_fma_f32 v[16:17], v[18:19], v[20:21], v[16:17] op_sel_hi:[1,0,1]
	s_nop 0
	v_mov_b32_e32 v23, v17
	v_pk_add_f32 v[16:17], v[26:27], v[22:23]
	v_pk_add_f32 v[18:19], v[26:27], v[22:23] neg_lo:[0,1] neg_hi:[0,1]
	ds_write_b128 v160, v[16:19] offset:24576
	ds_read_b128 v[16:19], v161 offset:32768
	s_waitcnt lgkmcnt(0)
; __device__ __forceinline__ void lds_barrier() { asm volatile("s_waitcnt lgkmcnt(0)" ::: "memory"); __builtin_amdgcn_s_barrier(); asm volatile("" ::: "memory"); }
; template <int R, class XT, class TWT>
; __device__ __forceinline__ void dit_task(XT X, TWT tw, int s, int task) {
;     const int lgM = 13 - s, lgq = lgM - R, q = 1 << lgq;
;     const int j0 = task & (q - 1), blk = task >> lgq, base = (blk << lgM) + j0;
;     const int pb = PADI(base), qp = (q >= 32) ? q + (q >> 4) : q;
;     f32x2v v[1 << R];
; #pragma unroll
;     for (int k = 0; k < (1 << R); ++k) v[k] = X[pb + k * qp];
; #pragma unroll
;     for (int r = R - 1; r >= 0; --r) {
;         const int pb = R - 1 - r;
; #pragma unroll
;         for (int k = 0; k < (1 << R); ++k) if (!((k >> pb) & 1)) {
;             const int klo = k & ((1 << pb) - 1);
;             const f32x2v w = tw[(j0 + (klo << lgq)) << (s + r)];
;             const f32x2v a = v[k], qv = v[k + (1 << pb)]; const f32x2v b = (f32x2v){qv.x * w.x + qv.y * w.y, qv.y * w.x - qv.x * w.y};
;             v[k] = a + b; v[k + (1 << pb)] = a - b;
;         }
;     }
; #pragma unroll
;     for (int k = 0; k < (1 << R); ++k) X[pb + k * qp] = v[k];
; }
; template <bool LAT>
; __device__ __forceinline__ void hyconv_unit(const Frame& F, LAS f32x2v* X, const TwHalf tw, LAS bf16* OUT, const float* skip, bf16* MIX, int u) {
;     ...
;             for (int r = 0; r < 8; ++r) { const int e = 2 * (F.tid + 512 * r);
;                 const f32x2v a = X[PADI(e)], b = X[PADI(e + 1)]; const f32x4 k = kq[r];
;                 const f32x2v p = a + b, q = a - b; const f32x2v pk = (f32x2v){p.x * k.x - p.y * k.y, p.x * k.y + p.y * k.x}, qk = (f32x2v){q.x * k.z - q.y * k.w, q.x * k.w + q.y * k.z};
;                 X[PADI(e)] = pk + qk; X[PADI(e + 1)] = pk - qk; }
;             lds_barrier();
	v_pk_add_f32 v[20:21], v[16:17], v[18:19]
	v_pk_add_f32 v[16:17], v[16:17], v[18:19] neg_lo:[0,1] neg_hi:[0,1]
	s_waitcnt vmcnt(3)
	v_pk_mul_f32 v[18:19], v[12:13], v[20:21] op_sel:[1,1] op_sel_hi:[0,1]
	v_pk_fma_f32 v[22:23], v[12:13], v[20:21], v[18:19] neg_lo:[0,0,1] neg_hi:[0,0,1]
	v_pk_fma_f32 v[12:13], v[12:13], v[20:21], v[18:19] op_sel_hi:[1,0,1]
	s_nop 0
	v_mov_b32_e32 v23, v13
	v_pk_mul_f32 v[12:13], v[14:15], v[16:17] op_sel:[1,1] op_sel_hi:[0,1]
	v_pk_fma_f32 v[18:19], v[14:15], v[16:17], v[12:13] neg_lo:[0,0,1] neg_hi:[0,0,1]
	v_pk_fma_f32 v[12:13], v[14:15], v[16:17], v[12:13] op_sel_hi:[1,0,1]
	s_nop 0
	v_mov_b32_e32 v19, v13
	v_pk_add_f32 v[12:13], v[22:23], v[18:19]
	v_pk_add_f32 v[14:15], v[22:23], v[18:19] neg_lo:[0,1] neg_hi:[0,1]
	ds_write_b128 v161, v[12:15] offset:32768
	ds_read_b128 v[12:15], v162 offset:40960
	s_waitcnt lgkmcnt(0)
	v_pk_add_f32 v[16:17], v[12:13], v[14:15]
	v_pk_add_f32 v[12:13], v[12:13], v[14:15] neg_lo:[0,1] neg_hi:[0,1]
	s_waitcnt vmcnt(2)
	v_pk_mul_f32 v[14:15], v[8:9], v[16:17] op_sel:[1,1] op_sel_hi:[0,1]
	v_pk_fma_f32 v[18:19], v[8:9], v[16:17], v[14:15] neg_lo:[0,0,1] neg_hi:[0,0,1]
	v_pk_fma_f32 v[8:9], v[8:9], v[16:17], v[14:15] op_sel_hi:[1,0,1]
	s_nop 0
	v_mov_b32_e32 v19, v9
	v_pk_mul_f32 v[8:9], v[10:11], v[12:13] op_sel:[1,1] op_sel_hi:[0,1]
	v_pk_fma_f32 v[14:15], v[10:11], v[12:13], v[8:9] neg_lo:[0,0,1] neg_hi:[0,0,1]
	v_pk_fma_f32 v[8:9], v[10:11], v[12:13], v[8:9] op_sel_hi:[1,0,1]
	s_nop 0
	v_mov_b32_e32 v15, v9
	v_pk_add_f32 v[8:9], v[18:19], v[14:15]
	v_pk_add_f32 v[10:11], v[18:19], v[14:15] neg_lo:[0,1] neg_hi:[0,1]
	ds_write_b128 v162, v[8:11] offset:40960
	ds_read_b128 v[8:11], v163 offset:49152
	s_waitcnt lgkmcnt(0)
	v_pk_add_f32 v[12:13], v[8:9], v[10:11]
	v_pk_add_f32 v[8:9], v[8:9], v[10:11] neg_lo:[0,1] neg_hi:[0,1]
	s_waitcnt vmcnt(1)
	v_pk_mul_f32 v[10:11], v[4:5], v[12:13] op_sel:[1,1] op_sel_hi:[0,1]
	v_pk_fma_f32 v[14:15], v[4:5], v[12:13], v[10:11] neg_lo:[0,0,1] neg_hi:[0,0,1]
	v_pk_fma_f32 v[4:5], v[4:5], v[12:13], v[10:11] op_sel_hi:[1,0,1]
	s_nop 0
	v_mov_b32_e32 v15, v5
	v_pk_mul_f32 v[4:5], v[6:7], v[8:9] op_sel:[1,1] op_sel_hi:[0,1]
	v_pk_fma_f32 v[10:11], v[6:7], v[8:9], v[4:5] neg_lo:[0,0,1] neg_hi:[0,0,1]
	v_pk_fma_f32 v[4:5], v[6:7], v[8:9], v[4:5] op_sel_hi:[1,0,1]
	s_nop 0
	v_mov_b32_e32 v11, v5
	v_pk_add_f32 v[4:5], v[14:15], v[10:11]
	v_pk_add_f32 v[6:7], v[14:15], v[10:11] neg_lo:[0,1] neg_hi:[0,1]
	ds_write_b128 v163, v[4:7] offset:49152
	ds_read_b128 v[4:7], v164 offset:57344
	s_waitcnt lgkmcnt(0)
	v_pk_add_f32 v[8:9], v[4:5], v[6:7]
	v_pk_add_f32 v[4:5], v[4:5], v[6:7] neg_lo:[0,1] neg_hi:[0,1]
	s_waitcnt vmcnt(0)
	v_pk_mul_f32 v[6:7], v[0:1], v[8:9] op_sel:[1,1] op_sel_hi:[0,1]
	v_pk_fma_f32 v[10:11], v[0:1], v[8:9], v[6:7] neg_lo:[0,0,1] neg_hi:[0,0,1]
	v_pk_fma_f32 v[0:1], v[0:1], v[8:9], v[6:7] op_sel_hi:[1,0,1]
	s_nop 0
	v_mov_b32_e32 v11, v1
	v_pk_mul_f32 v[0:1], v[2:3], v[4:5] op_sel:[1,1] op_sel_hi:[0,1]
	v_pk_fma_f32 v[6:7], v[2:3], v[4:5], v[0:1] neg_lo:[0,0,1] neg_hi:[0,0,1]
	v_pk_fma_f32 v[0:1], v[2:3], v[4:5], v[0:1] op_sel_hi:[1,0,1]
	s_nop 0
	v_mov_b32_e32 v7, v1
	v_pk_add_f32 v[0:1], v[10:11], v[6:7]
	v_pk_add_f32 v[2:3], v[10:11], v[6:7] neg_lo:[0,1] neg_hi:[0,1]
	ds_write_b128 v164, v[0:3] offset:57344
	s_waitcnt lgkmcnt(0)
	s_barrier
	ds_read2_b64 v[0:3], v137 offset1:2
	ds_read2_b64 v[4:7], v137 offset0:4 offset1:6
	ds_read2_b64 v[8:11], v137 offset0:8 offset1:10
	ds_read2_b64 v[12:15], v137 offset0:12 offset1:14
	ds_read2_b64 v[16:19], v137 offset0:16 offset1:18
	ds_read2_b64 v[20:23], v137 offset0:20 offset1:22
	ds_read2_b64 v[24:27], v137 offset0:24 offset1:26
	ds_read2_b64 v[28:31], v137 offset0:28 offset1:30
	ds_read_b64 v[104:105], v99
	ds_read_b64 v[106:107], v175
	ds_read_b64 v[108:109], v174
	ds_read2st64_b64 v[100:103], v170 offset1:16
	ds_read_b64 v[110:111], v173
	ds_read_b64 v[112:113], v156
	ds_read_b64 v[114:115], v171
	ds_read_b64 v[116:117], v172
	s_waitcnt lgkmcnt(7)
	v_xor_b32_e32 v99, 0x80000000, v104
	v_cndmask_b32_e64 v119, v99, v105, s[42:43]
	v_cndmask_b32_e64 v118, v105, v104, s[42:43]
	v_mov_b32_e32 v104, v119
	v_pk_mul_f32 v[120:121], v[2:3], v[104:105] op_sel_hi:[1,0]
	s_nop 0
	v_pk_fma_f32 v[122:123], v[2:3], v[118:119], v[120:121] op_sel:[0,0,1] op_sel_hi:[1,1,0]
	v_pk_fma_f32 v[2:3], v[2:3], v[118:119], v[120:121] op_sel:[0,0,1] op_sel_hi:[1,0,0] neg_lo:[0,0,1] neg_hi:[0,0,1]
	v_pk_mul_f32 v[120:121], v[6:7], v[104:105] op_sel_hi:[1,0]
	v_mov_b32_e32 v123, v3
	v_pk_fma_f32 v[124:125], v[6:7], v[118:119], v[120:121] op_sel:[0,0,1] op_sel_hi:[1,1,0]
	v_pk_fma_f32 v[6:7], v[6:7], v[118:119], v[120:121] op_sel:[0,0,1] op_sel_hi:[1,0,0] neg_lo:[0,0,1] neg_hi:[0,0,1]
	v_pk_add_f32 v[2:3], v[0:1], v[122:123]
	v_mov_b32_e32 v125, v7
	v_pk_add_f32 v[6:7], v[4:5], v[124:125]
	v_pk_add_f32 v[4:5], v[4:5], v[124:125] neg_lo:[0,1] neg_hi:[0,1]
	s_waitcnt lgkmcnt(6)
; template <int R, class XT, class TWT>
; __device__ __forceinline__ void dit_task(XT X, TWT tw, int s, int task) {
;     const int lgM = 13 - s, lgq = lgM - R, q = 1 << lgq;
;     const int j0 = task & (q - 1), blk = task >> lgq, base = (blk << lgM) + j0;
;     const int pb = PADI(base), qp = (q >= 32) ? q + (q >> 4) : q;
;     f32x2v v[1 << R];
; #pragma unroll
;     for (int k = 0; k < (1 << R); ++k) v[k] = X[pb + k * qp];
; #pragma unroll
;     for (int r = R - 1; r >= 0; --r) {
;         const int pb = R - 1 - r;
; #pragma unroll
;         for (int k = 0; k < (1 << R); ++k) if (!((k >> pb) & 1)) {
;             const int klo = k & ((1 << pb) - 1);
;             const f32x2v w = tw[(j0 + (klo << lgq)) << (s + r)];
;             const f32x2v a = v[k], qv = v[k + (1 << pb)]; const f32x2v b = (f32x2v){qv.x * w.x + qv.y * w.y, qv.y * w.x - qv.x * w.y};
;             v[k] = a + b; v[k + (1 << pb)] = a - b;
;         }
;     }
; #pragma unroll
;     for (int k = 0; k < (1 << R); ++k) X[pb + k * qp] = v[k];
	v_pk_mul_f32 v[120:121], v[106:107], v[6:7] op_sel:[1,0]
	v_pk_add_f32 v[0:1], v[0:1], v[122:123] neg_lo:[0,1] neg_hi:[0,1]
	v_pk_fma_f32 v[126:127], v[106:107], v[6:7], v[120:121] op_sel:[0,0,1] op_sel_hi:[1,1,0]
	v_pk_fma_f32 v[6:7], v[106:107], v[6:7], v[120:121] op_sel:[0,0,1] op_sel_hi:[0,1,0] neg_lo:[0,0,1] neg_hi:[0,0,1]
	v_pk_mul_f32 v[120:121], v[10:11], v[104:105] op_sel_hi:[1,0]
	v_mov_b32_e32 v127, v7
	v_pk_fma_f32 v[128:129], v[10:11], v[118:119], v[120:121] op_sel:[0,0,1] op_sel_hi:[1,1,0]
	v_pk_fma_f32 v[10:11], v[10:11], v[118:119], v[120:121] op_sel:[0,0,1] op_sel_hi:[1,0,0] neg_lo:[0,0,1] neg_hi:[0,0,1]
	v_pk_mul_f32 v[120:121], v[14:15], v[104:105] op_sel_hi:[1,0]
	v_mov_b32_e32 v129, v11
	v_pk_fma_f32 v[130:131], v[14:15], v[118:119], v[120:121] op_sel:[0,0,1] op_sel_hi:[1,1,0]
	v_pk_fma_f32 v[14:15], v[14:15], v[118:119], v[120:121] op_sel:[0,0,1] op_sel_hi:[1,0,0] neg_lo:[0,0,1] neg_hi:[0,0,1]
	v_pk_add_f32 v[10:11], v[8:9], v[128:129]
	v_mov_b32_e32 v131, v15
	v_pk_add_f32 v[14:15], v[12:13], v[130:131]
	v_pk_add_f32 v[12:13], v[12:13], v[130:131] neg_lo:[0,1] neg_hi:[0,1]
	v_pk_mul_f32 v[120:121], v[106:107], v[14:15] op_sel:[1,0]
	v_pk_add_f32 v[8:9], v[8:9], v[128:129] neg_lo:[0,1] neg_hi:[0,1]
	v_pk_fma_f32 v[132:133], v[106:107], v[14:15], v[120:121] op_sel:[0,0,1] op_sel_hi:[1,1,0]
	v_pk_fma_f32 v[14:15], v[106:107], v[14:15], v[120:121] op_sel:[0,0,1] op_sel_hi:[0,1,0] neg_lo:[0,0,1] neg_hi:[0,0,1]
	v_mov_b32_e32 v133, v15
	v_pk_add_f32 v[14:15], v[10:11], v[132:133]
	v_pk_add_f32 v[10:11], v[10:11], v[132:133] neg_lo:[0,1] neg_hi:[0,1]
	s_waitcnt lgkmcnt(3)
	v_pk_mul_f32 v[120:121], v[110:111], v[14:15] op_sel:[1,0]
	v_pk_add_f32 v[6:7], v[2:3], v[126:127]
	v_pk_fma_f32 v[176:177], v[110:111], v[14:15], v[120:121] op_sel:[0,0,1] op_sel_hi:[1,1,0]
	v_pk_fma_f32 v[14:15], v[110:111], v[14:15], v[120:121] op_sel:[0,0,1] op_sel_hi:[0,1,0] neg_lo:[0,0,1] neg_hi:[0,0,1]
	v_pk_mul_f32 v[120:121], v[18:19], v[104:105] op_sel_hi:[1,0]
	v_pk_add_f32 v[2:3], v[2:3], v[126:127] neg_lo:[0,1] neg_hi:[0,1]
	v_pk_fma_f32 v[178:179], v[18:19], v[118:119], v[120:121] op_sel:[0,0,1] op_sel_hi:[1,1,0]
	v_pk_fma_f32 v[18:19], v[18:19], v[118:119], v[120:121] op_sel:[0,0,1] op_sel_hi:[1,0,0] neg_lo:[0,0,1] neg_hi:[0,0,1]
	v_pk_mul_f32 v[120:121], v[22:23], v[104:105] op_sel_hi:[1,0]
	v_mov_b32_e32 v179, v19
	v_pk_fma_f32 v[182:183], v[22:23], v[118:119], v[120:121] op_sel:[0,0,1] op_sel_hi:[1,1,0]
	v_pk_fma_f32 v[22:23], v[22:23], v[118:119], v[120:121] op_sel:[0,0,1] op_sel_hi:[1,0,0] neg_lo:[0,0,1] neg_hi:[0,0,1]
	v_pk_add_f32 v[18:19], v[16:17], v[178:179]
	v_mov_b32_e32 v183, v23
	v_pk_add_f32 v[22:23], v[20:21], v[182:183]
	v_pk_add_f32 v[20:21], v[20:21], v[182:183] neg_lo:[0,1] neg_hi:[0,1]
	v_pk_mul_f32 v[120:121], v[106:107], v[22:23] op_sel:[1,0]
	v_pk_add_f32 v[16:17], v[16:17], v[178:179] neg_lo:[0,1] neg_hi:[0,1]
	v_pk_fma_f32 v[184:185], v[106:107], v[22:23], v[120:121] op_sel:[0,0,1] op_sel_hi:[1,1,0]
	v_pk_fma_f32 v[22:23], v[106:107], v[22:23], v[120:121] op_sel:[0,0,1] op_sel_hi:[0,1,0] neg_lo:[0,0,1] neg_hi:[0,0,1]
	v_pk_mul_f32 v[120:121], v[26:27], v[104:105] op_sel_hi:[1,0]
	v_pk_mul_f32 v[104:105], v[30:31], v[104:105] op_sel_hi:[1,0]
	v_pk_fma_f32 v[186:187], v[26:27], v[118:119], v[120:121] op_sel:[0,0,1] op_sel_hi:[1,1,0]
	v_pk_fma_f32 v[26:27], v[26:27], v[118:119], v[120:121] op_sel:[0,0,1] op_sel_hi:[1,0,0] neg_lo:[0,0,1] neg_hi:[0,0,1]
	v_pk_fma_f32 v[120:121], v[30:31], v[118:119], v[104:105] op_sel:[0,0,1] op_sel_hi:[1,1,0]
	v_pk_fma_f32 v[30:31], v[30:31], v[118:119], v[104:105] op_sel:[0,0,1] op_sel_hi:[1,0,0] neg_lo:[0,0,1] neg_hi:[0,0,1]
	v_mov_b32_e32 v187, v27
	v_mov_b32_e32 v121, v31
	v_pk_add_f32 v[30:31], v[28:29], v[120:121]
	v_pk_add_f32 v[26:27], v[24:25], v[186:187]
	v_pk_mul_f32 v[104:105], v[106:107], v[30:31] op_sel:[1,0]
	v_mov_b32_e32 v185, v23
	v_pk_fma_f32 v[118:119], v[106:107], v[30:31], v[104:105] op_sel:[0,0,1] op_sel_hi:[1,1,0]
	v_pk_fma_f32 v[30:31], v[106:107], v[30:31], v[104:105] op_sel:[0,0,1] op_sel_hi:[0,1,0] neg_lo:[0,0,1] neg_hi:[0,0,1]
	v_mov_b32_e32 v119, v31
	v_pk_add_f32 v[30:31], v[26:27], v[118:119]
	v_pk_add_f32 v[22:23], v[18:19], v[184:185]
	v_pk_mul_f32 v[104:105], v[110:111], v[30:31] op_sel:[1,0]
	v_pk_add_f32 v[28:29], v[28:29], v[120:121] neg_lo:[0,1] neg_hi:[0,1]
	v_pk_fma_f32 v[188:189], v[110:111], v[30:31], v[104:105] op_sel:[0,0,1] op_sel_hi:[1,1,0]
	v_pk_fma_f32 v[30:31], v[110:111], v[30:31], v[104:105] op_sel:[0,0,1] op_sel_hi:[0,1,0] neg_lo:[0,0,1] neg_hi:[0,0,1]
	v_mov_b32_e32 v189, v31
	v_pk_add_f32 v[30:31], v[22:23], v[188:189]
	v_pk_add_f32 v[24:25], v[24:25], v[186:187] neg_lo:[0,1] neg_hi:[0,1]
	v_pk_mul_f32 v[104:105], v[100:101], v[30:31] op_sel:[1,0]
	v_pk_add_f32 v[26:27], v[26:27], v[118:119] neg_lo:[0,1] neg_hi:[0,1]
	v_pk_fma_f32 v[190:191], v[100:101], v[30:31], v[104:105] op_sel:[0,0,1] op_sel_hi:[1,1,0]
	v_pk_fma_f32 v[30:31], v[100:101], v[30:31], v[104:105] op_sel:[0,0,1] op_sel_hi:[0,1,0] neg_lo:[0,0,1] neg_hi:[0,0,1]
	v_pk_mul_f32 v[104:105], v[106:107], v[4:5] op_sel_hi:[0,1]
	v_pk_fma_f32 v[122:123], v[106:107], v[4:5], v[104:105] op_sel:[1,0,1] op_sel_hi:[1,1,0] neg_lo:[0,0,1] neg_hi:[0,0,1]
	v_pk_fma_f32 v[4:5], v[106:107], v[4:5], v[104:105] op_sel:[1,0,1] op_sel_hi:[1,1,0]
	v_pk_mul_f32 v[104:105], v[106:107], v[12:13] op_sel_hi:[0,1]
	v_pk_fma_f32 v[124:125], v[106:107], v[12:13], v[104:105] op_sel:[1,0,1] op_sel_hi:[1,1,0] neg_lo:[0,0,1] neg_hi:[0,0,1]
	v_pk_fma_f32 v[12:13], v[106:107], v[12:13], v[104:105] op_sel:[1,0,1] op_sel_hi:[1,1,0]
	v_mov_b32_e32 v123, v5
	v_mov_b32_e32 v125, v13
; template <int R, class XT, class TWT>
; __device__ __forceinline__ void dit_task(XT X, TWT tw, int s, int task) {
;     const int lgM = 13 - s, lgq = lgM - R, q = 1 << lgq;
;     const int j0 = task & (q - 1), blk = task >> lgq, base = (blk << lgM) + j0;
;     const int pb = PADI(base), qp = (q >= 32) ? q + (q >> 4) : q;
;     f32x2v v[1 << R];
; #pragma unroll
;     for (int k = 0; k < (1 << R); ++k) v[k] = X[pb + k * qp];
; #pragma unroll
;     for (int r = R - 1; r >= 0; --r) {
;         const int pb = R - 1 - r;
; #pragma unroll
;         for (int k = 0; k < (1 << R); ++k) if (!((k >> pb) & 1)) {
;             const int klo = k & ((1 << pb) - 1);
;             const f32x2v w = tw[(j0 + (klo << lgq)) << (s + r)];
;             const f32x2v a = v[k], qv = v[k + (1 << pb)]; const f32x2v b = (f32x2v){qv.x * w.x + qv.y * w.y, qv.y * w.x - qv.x * w.y};
;             v[k] = a + b; v[k + (1 << pb)] = a - b;
;         }
;     }
; #pragma unroll
;     for (int k = 0; k < (1 << R); ++k) X[pb + k * qp] = v[k];
	v_pk_add_f32 v[12:13], v[8:9], v[124:125]
	v_pk_add_f32 v[4:5], v[0:1], v[122:123]
	v_pk_mul_f32 v[104:105], v[108:109], v[12:13] op_sel:[1,0]
	v_pk_add_f32 v[18:19], v[18:19], v[184:185] neg_lo:[0,1] neg_hi:[0,1]
	v_pk_fma_f32 v[128:129], v[108:109], v[12:13], v[104:105] op_sel:[0,0,1] op_sel_hi:[1,1,0]
	v_pk_fma_f32 v[12:13], v[108:109], v[12:13], v[104:105] op_sel:[0,0,1] op_sel_hi:[0,1,0] neg_lo:[0,0,1] neg_hi:[0,0,1]
	v_pk_mul_f32 v[104:105], v[106:107], v[20:21] op_sel_hi:[0,1]
	v_pk_fma_f32 v[130:131], v[106:107], v[20:21], v[104:105] op_sel:[1,0,1] op_sel_hi:[1,1,0] neg_lo:[0,0,1] neg_hi:[0,0,1]
	v_pk_fma_f32 v[20:21], v[106:107], v[20:21], v[104:105] op_sel:[1,0,1] op_sel_hi:[1,1,0]
	v_pk_mul_f32 v[104:105], v[106:107], v[28:29] op_sel_hi:[0,1]
	v_pk_fma_f32 v[120:121], v[106:107], v[28:29], v[104:105] op_sel:[1,0,1] op_sel_hi:[1,1,0] neg_lo:[0,0,1] neg_hi:[0,0,1]
	v_pk_fma_f32 v[28:29], v[106:107], v[28:29], v[104:105] op_sel:[1,0,1] op_sel_hi:[1,1,0]
	v_mov_b32_e32 v131, v21
	v_mov_b32_e32 v121, v29
	v_pk_add_f32 v[28:29], v[24:25], v[120:121]
	v_pk_add_f32 v[20:21], v[16:17], v[130:131]
	v_pk_mul_f32 v[104:105], v[108:109], v[28:29] op_sel:[1,0]
	v_mov_b32_e32 v129, v13
	v_pk_fma_f32 v[106:107], v[108:109], v[28:29], v[104:105] op_sel:[0,0,1] op_sel_hi:[1,1,0]
	v_pk_fma_f32 v[28:29], v[108:109], v[28:29], v[104:105] op_sel:[0,0,1] op_sel_hi:[0,1,0] neg_lo:[0,0,1] neg_hi:[0,0,1]
	v_mov_b32_e32 v107, v29
	v_pk_add_f32 v[28:29], v[20:21], v[106:107]
	v_pk_add_f32 v[12:13], v[4:5], v[128:129]
	s_waitcnt lgkmcnt(1)
	v_pk_mul_f32 v[104:105], v[114:115], v[28:29] op_sel:[1,0]
	v_pk_add_f32 v[8:9], v[8:9], v[124:125] neg_lo:[0,1] neg_hi:[0,1]
	v_pk_fma_f32 v[108:109], v[114:115], v[28:29], v[104:105] op_sel:[0,0,1] op_sel_hi:[1,1,0]
	v_pk_fma_f32 v[28:29], v[114:115], v[28:29], v[104:105] op_sel:[0,0,1] op_sel_hi:[0,1,0] neg_lo:[0,0,1] neg_hi:[0,0,1]
	v_mov_b32_e32 v109, v29
	v_pk_mul_f32 v[104:105], v[110:111], v[10:11] op_sel_hi:[0,1]
	v_pk_add_f32 v[28:29], v[12:13], v[108:109]
	v_pk_add_f32 v[12:13], v[12:13], v[108:109] neg_lo:[0,1] neg_hi:[0,1]
	v_pk_fma_f32 v[108:109], v[110:111], v[10:11], v[104:105] op_sel:[1,0,1] op_sel_hi:[1,1,0] neg_lo:[0,0,1] neg_hi:[0,0,1]
	v_pk_fma_f32 v[10:11], v[110:111], v[10:11], v[104:105] op_sel:[1,0,1] op_sel_hi:[1,1,0]
	v_pk_mul_f32 v[104:105], v[110:111], v[26:27] op_sel_hi:[0,1]
	v_pk_fma_f32 v[118:119], v[110:111], v[26:27], v[104:105] op_sel:[1,0,1] op_sel_hi:[1,1,0] neg_lo:[0,0,1] neg_hi:[0,0,1]
	v_pk_fma_f32 v[26:27], v[110:111], v[26:27], v[104:105] op_sel:[1,0,1] op_sel_hi:[1,1,0]
	v_mov_b32_e32 v109, v11
	v_mov_b32_e32 v119, v27
	v_pk_add_f32 v[26:27], v[18:19], v[118:119]
	v_pk_add_f32 v[10:11], v[2:3], v[108:109]
	v_pk_mul_f32 v[104:105], v[102:103], v[26:27] op_sel:[1,0]
	v_pk_add_f32 v[24:25], v[24:25], v[120:121] neg_lo:[0,1] neg_hi:[0,1]
	v_pk_fma_f32 v[110:111], v[102:103], v[26:27], v[104:105] op_sel:[0,0,1] op_sel_hi:[1,1,0]
	v_pk_fma_f32 v[26:27], v[102:103], v[26:27], v[104:105] op_sel:[0,0,1] op_sel_hi:[0,1,0] neg_lo:[0,0,1] neg_hi:[0,0,1]
	v_mov_b32_e32 v111, v27
	v_pk_mul_f32 v[104:105], v[112:113], v[8:9] op_sel_hi:[0,1]
	v_pk_add_f32 v[26:27], v[10:11], v[110:111]
	v_pk_add_f32 v[10:11], v[10:11], v[110:111] neg_lo:[0,1] neg_hi:[0,1]
	v_pk_fma_f32 v[110:111], v[112:113], v[8:9], v[104:105] op_sel:[1,0,1] op_sel_hi:[1,1,0] neg_lo:[0,0,1] neg_hi:[0,0,1]
	v_pk_fma_f32 v[8:9], v[112:113], v[8:9], v[104:105] op_sel:[1,0,1] op_sel_hi:[1,1,0]
	v_pk_mul_f32 v[104:105], v[112:113], v[24:25] op_sel_hi:[0,1]
	v_pk_fma_f32 v[120:121], v[112:113], v[24:25], v[104:105] op_sel:[1,0,1] op_sel_hi:[1,1,0] neg_lo:[0,0,1] neg_hi:[0,0,1]
	v_pk_fma_f32 v[24:25], v[112:113], v[24:25], v[104:105] op_sel:[1,0,1] op_sel_hi:[1,1,0]
	v_pk_add_f32 v[16:17], v[16:17], v[130:131] neg_lo:[0,1] neg_hi:[0,1]
	v_mov_b32_e32 v121, v25
	v_pk_add_f32 v[24:25], v[16:17], v[120:121]
	v_pk_add_f32 v[0:1], v[0:1], v[122:123] neg_lo:[0,1] neg_hi:[0,1]
	s_waitcnt lgkmcnt(0)
	v_pk_mul_f32 v[104:105], v[116:117], v[24:25] op_sel:[1,0]
	v_mov_b32_e32 v111, v9
	v_pk_fma_f32 v[112:113], v[116:117], v[24:25], v[104:105] op_sel:[0,0,1] op_sel_hi:[1,1,0]
	v_pk_fma_f32 v[24:25], v[116:117], v[24:25], v[104:105] op_sel:[0,0,1] op_sel_hi:[0,1,0] neg_lo:[0,0,1] neg_hi:[0,0,1]
	v_pk_add_f32 v[22:23], v[22:23], v[188:189] neg_lo:[0,1] neg_hi:[0,1]
	v_pk_add_f32 v[8:9], v[0:1], v[110:111]
	v_mov_b32_e32 v113, v25
	v_pk_mul_f32 v[104:105], v[100:101], v[22:23] op_sel_hi:[0,1]
	v_pk_add_f32 v[20:21], v[20:21], v[106:107] neg_lo:[0,1] neg_hi:[0,1]
	v_pk_add_f32 v[24:25], v[8:9], v[112:113]
	v_pk_add_f32 v[8:9], v[8:9], v[112:113] neg_lo:[0,1] neg_hi:[0,1]
	v_pk_fma_f32 v[112:113], v[100:101], v[22:23], v[104:105] op_sel:[1,0,1] op_sel_hi:[1,1,0] neg_lo:[0,0,1] neg_hi:[0,0,1]
	v_pk_fma_f32 v[22:23], v[100:101], v[22:23], v[104:105] op_sel:[1,0,1] op_sel_hi:[1,1,0]
	v_pk_mul_f32 v[100:101], v[114:115], v[20:21] op_sel_hi:[0,1]
	v_pk_fma_f32 v[104:105], v[114:115], v[20:21], v[100:101] op_sel:[1,0,1] op_sel_hi:[1,1,0] neg_lo:[0,0,1] neg_hi:[0,0,1]
	v_pk_fma_f32 v[20:21], v[114:115], v[20:21], v[100:101] op_sel:[1,0,1] op_sel_hi:[1,1,0]
	v_pk_add_f32 v[18:19], v[18:19], v[118:119] neg_lo:[0,1] neg_hi:[0,1]
	v_pk_add_f32 v[4:5], v[4:5], v[128:129] neg_lo:[0,1] neg_hi:[0,1]
	v_mov_b32_e32 v105, v21
	v_pk_mul_f32 v[100:101], v[102:103], v[18:19] op_sel_hi:[0,1]
	v_pk_add_f32 v[16:17], v[16:17], v[120:121] neg_lo:[0,1] neg_hi:[0,1]
	v_mov_b32_e32 v177, v15
	v_pk_add_f32 v[20:21], v[4:5], v[104:105]
	v_pk_add_f32 v[4:5], v[4:5], v[104:105] neg_lo:[0,1] neg_hi:[0,1]
	v_pk_fma_f32 v[104:105], v[102:103], v[18:19], v[100:101] op_sel:[1,0,1] op_sel_hi:[1,1,0] neg_lo:[0,0,1] neg_hi:[0,0,1]
; #define LAS __attribute__((address_space(3)))
; __device__ __forceinline__ void lds_barrier() { asm volatile("s_waitcnt lgkmcnt(0)" ::: "memory"); __builtin_amdgcn_s_barrier(); asm volatile("" ::: "memory"); }
; template <int R, class XT, class TWT>
; __device__ __forceinline__ void dit_task(XT X, TWT tw, int s, int task) {
;     const int lgM = 13 - s, lgq = lgM - R, q = 1 << lgq;
;     const int j0 = task & (q - 1), blk = task >> lgq, base = (blk << lgM) + j0;
;     const int pb = PADI(base), qp = (q >= 32) ? q + (q >> 4) : q;
;     f32x2v v[1 << R];
; #pragma unroll
;     for (int k = 0; k < (1 << R); ++k) v[k] = X[pb + k * qp];
; #pragma unroll
;     for (int r = R - 1; r >= 0; --r) {
;         const int pb = R - 1 - r;
; #pragma unroll
;         for (int k = 0; k < (1 << R); ++k) if (!((k >> pb) & 1)) {
;             const int klo = k & ((1 << pb) - 1);
;             const f32x2v w = tw[(j0 + (klo << lgq)) << (s + r)];
;             const f32x2v a = v[k], qv = v[k + (1 << pb)]; const f32x2v b = (f32x2v){qv.x * w.x + qv.y * w.y, qv.y * w.x - qv.x * w.y};
;             v[k] = a + b; v[k + (1 << pb)] = a - b;
;         }
;     }
; #pragma unroll
;     for (int k = 0; k < (1 << R); ++k) X[pb + k * qp] = v[k];
; __device__ __forceinline__ void fft_inv_upper(LAS f32x2v* X, TwHalf tw, int s0, int tid) {
;     dit_task<4>(X, tw, 8, tid); lds_barrier();
;     dit_task<4>(X, tw, 4, tid); lds_barrier();
;     if (s0 == 0) { dit_task<4>(X, tw, 0, tid); lds_barrier(); }
; }
	v_pk_fma_f32 v[18:19], v[102:103], v[18:19], v[100:101] op_sel:[1,0,1] op_sel_hi:[1,1,0]
	v_pk_mul_f32 v[100:101], v[116:117], v[16:17] op_sel_hi:[0,1]
	v_pk_add_f32 v[14:15], v[6:7], v[176:177]
	v_mov_b32_e32 v191, v31
	v_pk_fma_f32 v[102:103], v[116:117], v[16:17], v[100:101] op_sel:[1,0,1] op_sel_hi:[1,1,0] neg_lo:[0,0,1] neg_hi:[0,0,1]
	v_pk_fma_f32 v[16:17], v[116:117], v[16:17], v[100:101] op_sel:[1,0,1] op_sel_hi:[1,1,0]
	v_pk_add_f32 v[30:31], v[14:15], v[190:191]
	v_pk_add_f32 v[6:7], v[6:7], v[176:177] neg_lo:[0,1] neg_hi:[0,1]
	v_mov_b32_e32 v113, v23
	v_pk_add_f32 v[2:3], v[2:3], v[108:109] neg_lo:[0,1] neg_hi:[0,1]
	v_mov_b32_e32 v105, v19
	v_pk_add_f32 v[0:1], v[0:1], v[110:111] neg_lo:[0,1] neg_hi:[0,1]
	v_mov_b32_e32 v103, v17
	v_pk_add_f32 v[14:15], v[14:15], v[190:191] neg_lo:[0,1] neg_hi:[0,1]
	v_pk_add_f32 v[22:23], v[6:7], v[112:113]
	v_pk_add_f32 v[6:7], v[6:7], v[112:113] neg_lo:[0,1] neg_hi:[0,1]
	v_pk_add_f32 v[18:19], v[2:3], v[104:105]
	v_pk_add_f32 v[2:3], v[2:3], v[104:105] neg_lo:[0,1] neg_hi:[0,1]
	v_pk_add_f32 v[16:17], v[0:1], v[102:103]
	v_pk_add_f32 v[0:1], v[0:1], v[102:103] neg_lo:[0,1] neg_hi:[0,1]
	ds_write2_b64 v137, v[30:31], v[28:29] offset1:2
	ds_write2_b64 v137, v[26:27], v[24:25] offset0:4 offset1:6
	ds_write2_b64 v137, v[22:23], v[20:21] offset0:8 offset1:10
	ds_write2_b64 v137, v[18:19], v[16:17] offset0:12 offset1:14
	ds_write2_b64 v137, v[14:15], v[12:13] offset0:16 offset1:18
	ds_write2_b64 v137, v[10:11], v[8:9] offset0:20 offset1:22
	ds_write2_b64 v137, v[6:7], v[4:5] offset0:24 offset1:26
	ds_write2_b64 v137, v[2:3], v[0:1] offset0:28 offset1:30
	s_waitcnt lgkmcnt(0)
	s_barrier
	ds_read2_b64 v[0:3], v135 offset1:34
	ds_read2_b64 v[4:7], v135 offset0:68 offset1:102
	ds_read2_b64 v[8:11], v135 offset0:136 offset1:170
	ds_read2_b64 v[12:15], v135 offset0:204 offset1:238
	ds_read2_b64 v[16:19], v98 offset0:16 offset1:50
	ds_read2_b64 v[20:23], v98 offset0:84 offset1:118
	ds_read2_b64 v[24:27], v98 offset0:152 offset1:186
	ds_read2_b64 v[28:31], v98 offset0:220 offset1:254
	ds_read_b64 v[104:105], v136
	ds_read_b64 v[106:107], v169
	ds_read_b64 v[108:109], v167
	ds_read_b64 v[110:111], v168
	ds_read2st64_b64 v[100:103], v33 offset1:16
	ds_read_b64 v[112:113], v139
	ds_read_b64 v[114:115], v165
	ds_read_b64 v[116:117], v166
	s_waitcnt lgkmcnt(7)
	v_xor_b32_e32 v99, 0x80000000, v104
	v_cndmask_b32_e64 v119, v99, v105, s[44:45]
	v_cndmask_b32_e64 v118, v105, v104, s[44:45]
	v_mov_b32_e32 v104, v119
	v_pk_mul_f32 v[120:121], v[2:3], v[104:105] op_sel_hi:[1,0]
	s_nop 0
	v_pk_fma_f32 v[122:123], v[2:3], v[118:119], v[120:121] op_sel:[0,0,1] op_sel_hi:[1,1,0]
	v_pk_fma_f32 v[2:3], v[2:3], v[118:119], v[120:121] op_sel:[0,0,1] op_sel_hi:[1,0,0] neg_lo:[0,0,1] neg_hi:[0,0,1]
	v_pk_mul_f32 v[120:121], v[6:7], v[104:105] op_sel_hi:[1,0]
	v_mov_b32_e32 v123, v3
	v_pk_fma_f32 v[124:125], v[6:7], v[118:119], v[120:121] op_sel:[0,0,1] op_sel_hi:[1,1,0]
	v_pk_fma_f32 v[6:7], v[6:7], v[118:119], v[120:121] op_sel:[0,0,1] op_sel_hi:[1,0,0] neg_lo:[0,0,1] neg_hi:[0,0,1]
	v_pk_add_f32 v[2:3], v[0:1], v[122:123]
	v_mov_b32_e32 v125, v7
	v_pk_add_f32 v[6:7], v[4:5], v[124:125]
	v_pk_add_f32 v[4:5], v[4:5], v[124:125] neg_lo:[0,1] neg_hi:[0,1]
	s_waitcnt lgkmcnt(6)
	v_pk_mul_f32 v[120:121], v[106:107], v[6:7] op_sel:[1,0]
	v_pk_add_f32 v[0:1], v[0:1], v[122:123] neg_lo:[0,1] neg_hi:[0,1]
	v_pk_fma_f32 v[126:127], v[106:107], v[6:7], v[120:121] op_sel:[0,0,1] op_sel_hi:[1,1,0]
	v_pk_fma_f32 v[6:7], v[106:107], v[6:7], v[120:121] op_sel:[0,0,1] op_sel_hi:[0,1,0] neg_lo:[0,0,1] neg_hi:[0,0,1]
	v_pk_mul_f32 v[120:121], v[10:11], v[104:105] op_sel_hi:[1,0]
	v_mov_b32_e32 v127, v7
	v_pk_fma_f32 v[128:129], v[10:11], v[118:119], v[120:121] op_sel:[0,0,1] op_sel_hi:[1,1,0]
	v_pk_fma_f32 v[10:11], v[10:11], v[118:119], v[120:121] op_sel:[0,0,1] op_sel_hi:[1,0,0] neg_lo:[0,0,1] neg_hi:[0,0,1]
	v_pk_mul_f32 v[120:121], v[14:15], v[104:105] op_sel_hi:[1,0]
	v_mov_b32_e32 v129, v11
	v_pk_fma_f32 v[130:131], v[14:15], v[118:119], v[120:121] op_sel:[0,0,1] op_sel_hi:[1,1,0]
	v_pk_fma_f32 v[14:15], v[14:15], v[118:119], v[120:121] op_sel:[0,0,1] op_sel_hi:[1,0,0] neg_lo:[0,0,1] neg_hi:[0,0,1]
	v_pk_add_f32 v[10:11], v[8:9], v[128:129]
	v_mov_b32_e32 v131, v15
	v_pk_add_f32 v[14:15], v[12:13], v[130:131]
	v_pk_add_f32 v[12:13], v[12:13], v[130:131] neg_lo:[0,1] neg_hi:[0,1]
	v_pk_mul_f32 v[120:121], v[106:107], v[14:15] op_sel:[1,0]
	v_pk_add_f32 v[8:9], v[8:9], v[128:129] neg_lo:[0,1] neg_hi:[0,1]
	v_pk_fma_f32 v[132:133], v[106:107], v[14:15], v[120:121] op_sel:[0,0,1] op_sel_hi:[1,1,0]
	v_pk_fma_f32 v[14:15], v[106:107], v[14:15], v[120:121] op_sel:[0,0,1] op_sel_hi:[0,1,0] neg_lo:[0,0,1] neg_hi:[0,0,1]
	v_mov_b32_e32 v133, v15
	v_pk_add_f32 v[14:15], v[10:11], v[132:133]
	v_pk_add_f32 v[10:11], v[10:11], v[132:133] neg_lo:[0,1] neg_hi:[0,1]
	s_waitcnt lgkmcnt(5)
; template <int R, class XT, class TWT>
; __device__ __forceinline__ void dit_task(XT X, TWT tw, int s, int task) {
;     const int lgM = 13 - s, lgq = lgM - R, q = 1 << lgq;
;     const int j0 = task & (q - 1), blk = task >> lgq, base = (blk << lgM) + j0;
;     const int pb = PADI(base), qp = (q >= 32) ? q + (q >> 4) : q;
;     f32x2v v[1 << R];
; #pragma unroll
;     for (int k = 0; k < (1 << R); ++k) v[k] = X[pb + k * qp];
; #pragma unroll
;     for (int r = R - 1; r >= 0; --r) {
;         const int pb = R - 1 - r;
; #pragma unroll
;         for (int k = 0; k < (1 << R); ++k) if (!((k >> pb) & 1)) {
;             const int klo = k & ((1 << pb) - 1);
;             const f32x2v w = tw[(j0 + (klo << lgq)) << (s + r)];
;             const f32x2v a = v[k], qv = v[k + (1 << pb)]; const f32x2v b = (f32x2v){qv.x * w.x + qv.y * w.y, qv.y * w.x - qv.x * w.y};
;             v[k] = a + b; v[k + (1 << pb)] = a - b;
;         }
;     }
; #pragma unroll
;     for (int k = 0; k < (1 << R); ++k) X[pb + k * qp] = v[k];
	v_pk_mul_f32 v[120:121], v[108:109], v[14:15] op_sel:[1,0]
	v_pk_add_f32 v[6:7], v[2:3], v[126:127]
	v_pk_fma_f32 v[176:177], v[108:109], v[14:15], v[120:121] op_sel:[0,0,1] op_sel_hi:[1,1,0]
	v_pk_fma_f32 v[14:15], v[108:109], v[14:15], v[120:121] op_sel:[0,0,1] op_sel_hi:[0,1,0] neg_lo:[0,0,1] neg_hi:[0,0,1]
	v_pk_mul_f32 v[120:121], v[18:19], v[104:105] op_sel_hi:[1,0]
	v_pk_add_f32 v[2:3], v[2:3], v[126:127] neg_lo:[0,1] neg_hi:[0,1]
	v_pk_fma_f32 v[178:179], v[18:19], v[118:119], v[120:121] op_sel:[0,0,1] op_sel_hi:[1,1,0]
	v_pk_fma_f32 v[18:19], v[18:19], v[118:119], v[120:121] op_sel:[0,0,1] op_sel_hi:[1,0,0] neg_lo:[0,0,1] neg_hi:[0,0,1]
	v_pk_mul_f32 v[120:121], v[22:23], v[104:105] op_sel_hi:[1,0]
	v_mov_b32_e32 v179, v19
	v_pk_fma_f32 v[182:183], v[22:23], v[118:119], v[120:121] op_sel:[0,0,1] op_sel_hi:[1,1,0]
	v_pk_fma_f32 v[22:23], v[22:23], v[118:119], v[120:121] op_sel:[0,0,1] op_sel_hi:[1,0,0] neg_lo:[0,0,1] neg_hi:[0,0,1]
	v_pk_add_f32 v[18:19], v[16:17], v[178:179]
	v_mov_b32_e32 v183, v23
	v_pk_add_f32 v[22:23], v[20:21], v[182:183]
	v_pk_add_f32 v[20:21], v[20:21], v[182:183] neg_lo:[0,1] neg_hi:[0,1]
	v_pk_mul_f32 v[120:121], v[106:107], v[22:23] op_sel:[1,0]
	v_pk_add_f32 v[16:17], v[16:17], v[178:179] neg_lo:[0,1] neg_hi:[0,1]
	v_pk_fma_f32 v[184:185], v[106:107], v[22:23], v[120:121] op_sel:[0,0,1] op_sel_hi:[1,1,0]
	v_pk_fma_f32 v[22:23], v[106:107], v[22:23], v[120:121] op_sel:[0,0,1] op_sel_hi:[0,1,0] neg_lo:[0,0,1] neg_hi:[0,0,1]
	v_pk_mul_f32 v[120:121], v[26:27], v[104:105] op_sel_hi:[1,0]
	v_pk_mul_f32 v[104:105], v[30:31], v[104:105] op_sel_hi:[1,0]
	v_pk_fma_f32 v[186:187], v[26:27], v[118:119], v[120:121] op_sel:[0,0,1] op_sel_hi:[1,1,0]
	v_pk_fma_f32 v[26:27], v[26:27], v[118:119], v[120:121] op_sel:[0,0,1] op_sel_hi:[1,0,0] neg_lo:[0,0,1] neg_hi:[0,0,1]
	v_pk_fma_f32 v[120:121], v[30:31], v[118:119], v[104:105] op_sel:[0,0,1] op_sel_hi:[1,1,0]
	v_pk_fma_f32 v[30:31], v[30:31], v[118:119], v[104:105] op_sel:[0,0,1] op_sel_hi:[1,0,0] neg_lo:[0,0,1] neg_hi:[0,0,1]
	v_mov_b32_e32 v187, v27
	v_mov_b32_e32 v121, v31
	v_pk_add_f32 v[30:31], v[28:29], v[120:121]
	v_pk_add_f32 v[26:27], v[24:25], v[186:187]
	v_pk_mul_f32 v[104:105], v[106:107], v[30:31] op_sel:[1,0]
	v_mov_b32_e32 v185, v23
	v_pk_fma_f32 v[118:119], v[106:107], v[30:31], v[104:105] op_sel:[0,0,1] op_sel_hi:[1,1,0]
	v_pk_fma_f32 v[30:31], v[106:107], v[30:31], v[104:105] op_sel:[0,0,1] op_sel_hi:[0,1,0] neg_lo:[0,0,1] neg_hi:[0,0,1]
	v_mov_b32_e32 v119, v31
	v_pk_add_f32 v[30:31], v[26:27], v[118:119]
	v_pk_add_f32 v[22:23], v[18:19], v[184:185]
	v_pk_mul_f32 v[104:105], v[108:109], v[30:31] op_sel:[1,0]
	v_pk_add_f32 v[28:29], v[28:29], v[120:121] neg_lo:[0,1] neg_hi:[0,1]
	v_pk_fma_f32 v[188:189], v[108:109], v[30:31], v[104:105] op_sel:[0,0,1] op_sel_hi:[1,1,0]
	v_pk_fma_f32 v[30:31], v[108:109], v[30:31], v[104:105] op_sel:[0,0,1] op_sel_hi:[0,1,0] neg_lo:[0,0,1] neg_hi:[0,0,1]
	v_mov_b32_e32 v189, v31
	v_pk_add_f32 v[30:31], v[22:23], v[188:189]
	v_pk_add_f32 v[24:25], v[24:25], v[186:187] neg_lo:[0,1] neg_hi:[0,1]
	s_waitcnt lgkmcnt(3)
	v_pk_mul_f32 v[104:105], v[100:101], v[30:31] op_sel:[1,0]
	v_pk_add_f32 v[26:27], v[26:27], v[118:119] neg_lo:[0,1] neg_hi:[0,1]
	v_pk_fma_f32 v[190:191], v[100:101], v[30:31], v[104:105] op_sel:[0,0,1] op_sel_hi:[1,1,0]
	v_pk_fma_f32 v[30:31], v[100:101], v[30:31], v[104:105] op_sel:[0,0,1] op_sel_hi:[0,1,0] neg_lo:[0,0,1] neg_hi:[0,0,1]
	v_pk_mul_f32 v[104:105], v[106:107], v[4:5] op_sel_hi:[0,1]
	v_pk_fma_f32 v[122:123], v[106:107], v[4:5], v[104:105] op_sel:[1,0,1] op_sel_hi:[1,1,0] neg_lo:[0,0,1] neg_hi:[0,0,1]
	v_pk_fma_f32 v[4:5], v[106:107], v[4:5], v[104:105] op_sel:[1,0,1] op_sel_hi:[1,1,0]
	v_pk_mul_f32 v[104:105], v[106:107], v[12:13] op_sel_hi:[0,1]
	v_pk_fma_f32 v[124:125], v[106:107], v[12:13], v[104:105] op_sel:[1,0,1] op_sel_hi:[1,1,0] neg_lo:[0,0,1] neg_hi:[0,0,1]
	v_pk_fma_f32 v[12:13], v[106:107], v[12:13], v[104:105] op_sel:[1,0,1] op_sel_hi:[1,1,0]
	v_mov_b32_e32 v123, v5
	v_mov_b32_e32 v125, v13
	v_pk_add_f32 v[12:13], v[8:9], v[124:125]
	v_pk_add_f32 v[4:5], v[0:1], v[122:123]
	v_pk_mul_f32 v[104:105], v[110:111], v[12:13] op_sel:[1,0]
	v_pk_add_f32 v[18:19], v[18:19], v[184:185] neg_lo:[0,1] neg_hi:[0,1]
	v_pk_fma_f32 v[128:129], v[110:111], v[12:13], v[104:105] op_sel:[0,0,1] op_sel_hi:[1,1,0]
	v_pk_fma_f32 v[12:13], v[110:111], v[12:13], v[104:105] op_sel:[0,0,1] op_sel_hi:[0,1,0] neg_lo:[0,0,1] neg_hi:[0,0,1]
	v_pk_mul_f32 v[104:105], v[106:107], v[20:21] op_sel_hi:[0,1]
	v_pk_fma_f32 v[130:131], v[106:107], v[20:21], v[104:105] op_sel:[1,0,1] op_sel_hi:[1,1,0] neg_lo:[0,0,1] neg_hi:[0,0,1]
	v_pk_fma_f32 v[20:21], v[106:107], v[20:21], v[104:105] op_sel:[1,0,1] op_sel_hi:[1,1,0]
	v_pk_mul_f32 v[104:105], v[106:107], v[28:29] op_sel_hi:[0,1]
	v_pk_fma_f32 v[120:121], v[106:107], v[28:29], v[104:105] op_sel:[1,0,1] op_sel_hi:[1,1,0] neg_lo:[0,0,1] neg_hi:[0,0,1]
	v_pk_fma_f32 v[28:29], v[106:107], v[28:29], v[104:105] op_sel:[1,0,1] op_sel_hi:[1,1,0]
	v_mov_b32_e32 v131, v21
	v_mov_b32_e32 v121, v29
	v_pk_add_f32 v[28:29], v[24:25], v[120:121]
	v_pk_add_f32 v[20:21], v[16:17], v[130:131]
	v_pk_mul_f32 v[104:105], v[110:111], v[28:29] op_sel:[1,0]
	v_mov_b32_e32 v129, v13
	v_pk_fma_f32 v[106:107], v[110:111], v[28:29], v[104:105] op_sel:[0,0,1] op_sel_hi:[1,1,0]
	v_pk_fma_f32 v[28:29], v[110:111], v[28:29], v[104:105] op_sel:[0,0,1] op_sel_hi:[0,1,0] neg_lo:[0,0,1] neg_hi:[0,0,1]
	v_mov_b32_e32 v107, v29
	v_pk_add_f32 v[28:29], v[20:21], v[106:107]
	v_pk_add_f32 v[12:13], v[4:5], v[128:129]
	s_waitcnt lgkmcnt(1)
; template <int R, class XT, class TWT>
; __device__ __forceinline__ void dit_task(XT X, TWT tw, int s, int task) {
;     const int lgM = 13 - s, lgq = lgM - R, q = 1 << lgq;
;     const int j0 = task & (q - 1), blk = task >> lgq, base = (blk << lgM) + j0;
;     const int pb = PADI(base), qp = (q >= 32) ? q + (q >> 4) : q;
;     f32x2v v[1 << R];
; #pragma unroll
;     for (int k = 0; k < (1 << R); ++k) v[k] = X[pb + k * qp];
; #pragma unroll
;     for (int r = R - 1; r >= 0; --r) {
;         const int pb = R - 1 - r;
; #pragma unroll
;         for (int k = 0; k < (1 << R); ++k) if (!((k >> pb) & 1)) {
;             const int klo = k & ((1 << pb) - 1);
;             const f32x2v w = tw[(j0 + (klo << lgq)) << (s + r)];
;             const f32x2v a = v[k], qv = v[k + (1 << pb)]; const f32x2v b = (f32x2v){qv.x * w.x + qv.y * w.y, qv.y * w.x - qv.x * w.y};
;             v[k] = a + b; v[k + (1 << pb)] = a - b;
;         }
;     }
; #pragma unroll
;     for (int k = 0; k < (1 << R); ++k) X[pb + k * qp] = v[k];
	v_pk_mul_f32 v[104:105], v[114:115], v[28:29] op_sel:[1,0]
	v_pk_add_f32 v[8:9], v[8:9], v[124:125] neg_lo:[0,1] neg_hi:[0,1]
	v_pk_fma_f32 v[110:111], v[114:115], v[28:29], v[104:105] op_sel:[0,0,1] op_sel_hi:[1,1,0]
	v_pk_fma_f32 v[28:29], v[114:115], v[28:29], v[104:105] op_sel:[0,0,1] op_sel_hi:[0,1,0] neg_lo:[0,0,1] neg_hi:[0,0,1]
	v_mov_b32_e32 v111, v29
	v_pk_mul_f32 v[104:105], v[108:109], v[10:11] op_sel_hi:[0,1]
	v_pk_add_f32 v[28:29], v[12:13], v[110:111]
	v_pk_add_f32 v[12:13], v[12:13], v[110:111] neg_lo:[0,1] neg_hi:[0,1]
	v_pk_fma_f32 v[110:111], v[108:109], v[10:11], v[104:105] op_sel:[1,0,1] op_sel_hi:[1,1,0] neg_lo:[0,0,1] neg_hi:[0,0,1]
	v_pk_fma_f32 v[10:11], v[108:109], v[10:11], v[104:105] op_sel:[1,0,1] op_sel_hi:[1,1,0]
	v_pk_mul_f32 v[104:105], v[108:109], v[26:27] op_sel_hi:[0,1]
	v_pk_fma_f32 v[118:119], v[108:109], v[26:27], v[104:105] op_sel:[1,0,1] op_sel_hi:[1,1,0] neg_lo:[0,0,1] neg_hi:[0,0,1]
	v_pk_fma_f32 v[26:27], v[108:109], v[26:27], v[104:105] op_sel:[1,0,1] op_sel_hi:[1,1,0]
	v_mov_b32_e32 v111, v11
	v_mov_b32_e32 v119, v27
	v_pk_add_f32 v[26:27], v[18:19], v[118:119]
	v_pk_add_f32 v[10:11], v[2:3], v[110:111]
	v_pk_mul_f32 v[104:105], v[102:103], v[26:27] op_sel:[1,0]
	v_pk_add_f32 v[24:25], v[24:25], v[120:121] neg_lo:[0,1] neg_hi:[0,1]
	v_pk_fma_f32 v[108:109], v[102:103], v[26:27], v[104:105] op_sel:[0,0,1] op_sel_hi:[1,1,0]
	v_pk_fma_f32 v[26:27], v[102:103], v[26:27], v[104:105] op_sel:[0,0,1] op_sel_hi:[0,1,0] neg_lo:[0,0,1] neg_hi:[0,0,1]
	v_mov_b32_e32 v109, v27
	v_pk_mul_f32 v[104:105], v[112:113], v[8:9] op_sel_hi:[0,1]
	v_pk_add_f32 v[26:27], v[10:11], v[108:109]
	v_pk_add_f32 v[10:11], v[10:11], v[108:109] neg_lo:[0,1] neg_hi:[0,1]
	v_pk_fma_f32 v[108:109], v[112:113], v[8:9], v[104:105] op_sel:[1,0,1] op_sel_hi:[1,1,0] neg_lo:[0,0,1] neg_hi:[0,0,1]
	v_pk_fma_f32 v[8:9], v[112:113], v[8:9], v[104:105] op_sel:[1,0,1] op_sel_hi:[1,1,0]
	v_pk_mul_f32 v[104:105], v[112:113], v[24:25] op_sel_hi:[0,1]
	v_pk_fma_f32 v[120:121], v[112:113], v[24:25], v[104:105] op_sel:[1,0,1] op_sel_hi:[1,1,0] neg_lo:[0,0,1] neg_hi:[0,0,1]
	v_pk_fma_f32 v[24:25], v[112:113], v[24:25], v[104:105] op_sel:[1,0,1] op_sel_hi:[1,1,0]
	v_pk_add_f32 v[16:17], v[16:17], v[130:131] neg_lo:[0,1] neg_hi:[0,1]
	v_mov_b32_e32 v121, v25
	v_pk_add_f32 v[24:25], v[16:17], v[120:121]
	v_pk_add_f32 v[0:1], v[0:1], v[122:123] neg_lo:[0,1] neg_hi:[0,1]
	s_waitcnt lgkmcnt(0)
	v_pk_mul_f32 v[104:105], v[116:117], v[24:25] op_sel:[1,0]
	v_mov_b32_e32 v109, v9
	v_pk_fma_f32 v[112:113], v[116:117], v[24:25], v[104:105] op_sel:[0,0,1] op_sel_hi:[1,1,0]
	v_pk_fma_f32 v[24:25], v[116:117], v[24:25], v[104:105] op_sel:[0,0,1] op_sel_hi:[0,1,0] neg_lo:[0,0,1] neg_hi:[0,0,1]
	v_pk_add_f32 v[22:23], v[22:23], v[188:189] neg_lo:[0,1] neg_hi:[0,1]
	v_pk_add_f32 v[8:9], v[0:1], v[108:109]
	v_mov_b32_e32 v113, v25
	v_pk_mul_f32 v[104:105], v[100:101], v[22:23] op_sel_hi:[0,1]
	v_pk_add_f32 v[20:21], v[20:21], v[106:107] neg_lo:[0,1] neg_hi:[0,1]
	v_pk_add_f32 v[24:25], v[8:9], v[112:113]
	v_pk_add_f32 v[8:9], v[8:9], v[112:113] neg_lo:[0,1] neg_hi:[0,1]
	v_pk_fma_f32 v[112:113], v[100:101], v[22:23], v[104:105] op_sel:[1,0,1] op_sel_hi:[1,1,0] neg_lo:[0,0,1] neg_hi:[0,0,1]
	v_pk_fma_f32 v[22:23], v[100:101], v[22:23], v[104:105] op_sel:[1,0,1] op_sel_hi:[1,1,0]
	v_pk_mul_f32 v[100:101], v[114:115], v[20:21] op_sel_hi:[0,1]
	v_pk_fma_f32 v[104:105], v[114:115], v[20:21], v[100:101] op_sel:[1,0,1] op_sel_hi:[1,1,0] neg_lo:[0,0,1] neg_hi:[0,0,1]
	v_pk_fma_f32 v[20:21], v[114:115], v[20:21], v[100:101] op_sel:[1,0,1] op_sel_hi:[1,1,0]
	v_pk_add_f32 v[18:19], v[18:19], v[118:119] neg_lo:[0,1] neg_hi:[0,1]
	v_pk_add_f32 v[4:5], v[4:5], v[128:129] neg_lo:[0,1] neg_hi:[0,1]
	v_mov_b32_e32 v105, v21
	v_pk_mul_f32 v[100:101], v[102:103], v[18:19] op_sel_hi:[0,1]
	v_pk_add_f32 v[16:17], v[16:17], v[120:121] neg_lo:[0,1] neg_hi:[0,1]
	v_mov_b32_e32 v177, v15
	v_pk_add_f32 v[20:21], v[4:5], v[104:105]
	v_pk_add_f32 v[4:5], v[4:5], v[104:105] neg_lo:[0,1] neg_hi:[0,1]
	v_pk_fma_f32 v[104:105], v[102:103], v[18:19], v[100:101] op_sel:[1,0,1] op_sel_hi:[1,1,0] neg_lo:[0,0,1] neg_hi:[0,0,1]
	v_pk_fma_f32 v[18:19], v[102:103], v[18:19], v[100:101] op_sel:[1,0,1] op_sel_hi:[1,1,0]
	v_pk_mul_f32 v[100:101], v[116:117], v[16:17] op_sel_hi:[0,1]
	v_pk_add_f32 v[14:15], v[6:7], v[176:177]
	v_mov_b32_e32 v191, v31
	v_pk_fma_f32 v[102:103], v[116:117], v[16:17], v[100:101] op_sel:[1,0,1] op_sel_hi:[1,1,0] neg_lo:[0,0,1] neg_hi:[0,0,1]
	v_pk_fma_f32 v[16:17], v[116:117], v[16:17], v[100:101] op_sel:[1,0,1] op_sel_hi:[1,1,0]
	v_pk_add_f32 v[30:31], v[14:15], v[190:191]
	v_pk_add_f32 v[6:7], v[6:7], v[176:177] neg_lo:[0,1] neg_hi:[0,1]
	v_mov_b32_e32 v113, v23
	v_pk_add_f32 v[2:3], v[2:3], v[110:111] neg_lo:[0,1] neg_hi:[0,1]
	v_mov_b32_e32 v105, v19
	v_pk_add_f32 v[0:1], v[0:1], v[108:109] neg_lo:[0,1] neg_hi:[0,1]
	v_mov_b32_e32 v103, v17
	v_pk_add_f32 v[14:15], v[14:15], v[190:191] neg_lo:[0,1] neg_hi:[0,1]
	v_pk_add_f32 v[22:23], v[6:7], v[112:113]
	v_pk_add_f32 v[6:7], v[6:7], v[112:113] neg_lo:[0,1] neg_hi:[0,1]
	v_pk_add_f32 v[18:19], v[2:3], v[104:105]
	v_pk_add_f32 v[2:3], v[2:3], v[104:105] neg_lo:[0,1] neg_hi:[0,1]
	v_pk_add_f32 v[16:17], v[0:1], v[102:103]
	v_pk_add_f32 v[0:1], v[0:1], v[102:103] neg_lo:[0,1] neg_hi:[0,1]
	ds_write2_b64 v135, v[30:31], v[28:29] offset1:34
	ds_write2_b64 v135, v[26:27], v[24:25] offset0:68 offset1:102
	ds_write2_b64 v135, v[22:23], v[20:21] offset0:136 offset1:170
	ds_write2_b64 v135, v[18:19], v[16:17] offset0:204 offset1:238
	ds_write2_b64 v98, v[14:15], v[12:13] offset0:16 offset1:50
	ds_write2_b64 v98, v[10:11], v[8:9] offset0:84 offset1:118
	ds_write2_b64 v98, v[6:7], v[4:5] offset0:152 offset1:186
	ds_write2_b64 v98, v[2:3], v[0:1] offset0:220 offset1:254
	s_waitcnt lgkmcnt(0)
	s_barrier
; template <bool LAT>
; __device__ __forceinline__ void hyconv_unit(const Frame& F, LAS f32x2v* X, const TwHalf tw, LAS bf16* OUT, const float* skip, bf16* MIX, int u) {
;     ...
;                 f32x2v g[16], zp[16];
;                 { const bf16* g0 = H0 + (size_t)(ord * 256 + c0) * L + n; const bf16* g1 = H1 + (size_t)(ord * 256 + c0) * L + n; const bf16* v0 = H0 + (size_t)(512 + c0) * L + n; const bf16* v1 = H1 + (size_t)(512 + c0) * L + n;
; #pragma unroll
;                   for (int r = 0; r < 16; ++r) { g[r] = (f32x2v){0.f, 0.f}; zp[r] = g[r]; if (act) { g[r] = (f32x2v){bf2f(g0[r * L]), bf2f(g1[r * L])}; zp[r] = (f32x2v){bf2f(v0[r * L]), bf2f(v1[r * L])}; } } }
	v_lshl_add_u64 v[104:105], v[56:57], 0, s[90:91]
	v_lshl_add_u64 v[102:103], v[62:63], 0, s[90:91]
	v_mov_b32_e32 v2, 0
	v_mov_b32_e32 v3, 0
	v_mov_b32_e32 v4, 0
	v_mov_b32_e32 v5, 0
	v_mov_b32_e32 v0, 0
	v_mov_b32_e32 v1, 0
	v_mov_b32_e32 v6, 0
	v_mov_b32_e32 v7, 0
	v_mov_b32_e32 v10, 0
	v_mov_b32_e32 v11, 0
	v_mov_b32_e32 v12, 0
	v_mov_b32_e32 v13, 0
	v_mov_b32_e32 v8, 0
	v_mov_b32_e32 v9, 0
	v_mov_b32_e32 v14, 0
	v_mov_b32_e32 v15, 0
	v_mov_b32_e32 v18, 0
	v_mov_b32_e32 v19, 0
	v_mov_b32_e32 v20, 0
	v_mov_b32_e32 v21, 0
	v_mov_b32_e32 v16, 0
	v_mov_b32_e32 v17, 0
	v_mov_b32_e32 v22, 0
	v_mov_b32_e32 v23, 0
	v_mov_b32_e32 v26, 0
	v_mov_b32_e32 v27, 0
	v_mov_b32_e32 v28, 0
	v_mov_b32_e32 v29, 0
	v_mov_b32_e32 v24, 0
	v_mov_b32_e32 v25, 0
	v_mov_b32_e32 v98, 0
	v_mov_b32_e32 v99, 0
	v_mov_b32_e32 v100, 0
	v_mov_b32_e32 v101, 0
	v_mov_b32_e32 v106, 0
	v_mov_b32_e32 v107, 0
	v_mov_b32_e32 v30, 0
	v_mov_b32_e32 v31, 0
	v_mov_b32_e32 v108, 0
	v_mov_b32_e32 v109, 0
	v_mov_b32_e32 v112, 0
	v_mov_b32_e32 v113, 0
	v_mov_b32_e32 v114, 0
	v_mov_b32_e32 v115, 0
	v_mov_b32_e32 v110, 0
	v_mov_b32_e32 v111, 0
	v_mov_b32_e32 v116, 0
	v_mov_b32_e32 v117, 0
	v_mov_b32_e32 v120, 0
	v_mov_b32_e32 v121, 0
	v_mov_b32_e32 v122, 0
	v_mov_b32_e32 v123, 0
	v_mov_b32_e32 v118, 0
	v_mov_b32_e32 v119, 0
	v_mov_b32_e32 v124, 0
	v_mov_b32_e32 v125, 0
	v_mov_b32_e32 v128, 0
	v_mov_b32_e32 v129, 0
	v_mov_b32_e32 v130, 0
	v_mov_b32_e32 v131, 0
	v_mov_b32_e32 v126, 0
	v_mov_b32_e32 v127, 0
	v_mov_b32_e32 v132, 0
	v_mov_b32_e32 v133, 0
	s_and_saveexec_b64 s[0:1], s[38:39]
	s_mov_b64 s[2:3], 0x1000
	v_lshl_add_u64 v[192:193], v[104:105], 0, s[2:3]
	v_lshl_add_u64 v[194:195], v[102:103], 0, s[2:3]
	global_load_ushort v2, v[104:105], off
	global_load_ushort v3, v[102:103], off
	global_load_ushort v4, v[52:53], off
	global_load_ushort v5, v[54:55], off
	global_load_ushort v0, v[104:105], off offset:512
	global_load_ushort v1, v[102:103], off offset:512
	global_load_ushort v6, v[52:53], off offset:512
	global_load_ushort v7, v[54:55], off offset:512
	global_load_ushort v10, v[104:105], off offset:1024
	global_load_ushort v11, v[102:103], off offset:1024
	global_load_ushort v12, v[52:53], off offset:1024
	global_load_ushort v13, v[54:55], off offset:1024
	global_load_ushort v8, v[104:105], off offset:1536
	global_load_ushort v9, v[102:103], off offset:1536
	global_load_ushort v14, v[52:53], off offset:1536
	global_load_ushort v15, v[54:55], off offset:1536
	global_load_ushort v18, v[104:105], off offset:2048
	global_load_ushort v19, v[102:103], off offset:2048
	global_load_ushort v20, v[52:53], off offset:2048
	global_load_ushort v21, v[54:55], off offset:2048
	global_load_ushort v16, v[104:105], off offset:2560
	global_load_ushort v17, v[102:103], off offset:2560
	global_load_ushort v22, v[52:53], off offset:2560
	global_load_ushort v23, v[54:55], off offset:2560
	global_load_ushort v26, v[104:105], off offset:3072
	global_load_ushort v27, v[102:103], off offset:3072
	global_load_ushort v28, v[52:53], off offset:3072
	global_load_ushort v29, v[54:55], off offset:3072
	global_load_ushort v24, v[104:105], off offset:3584
	global_load_ushort v25, v[102:103], off offset:3584
	global_load_ushort v98, v[52:53], off offset:3584
	global_load_ushort v99, v[54:55], off offset:3584
	global_load_ushort v100, v[192:193], off
	global_load_ushort v101, v[194:195], off
	global_load_ushort v106, v[66:67], off
	global_load_ushort v107, v[68:69], off
	global_load_ushort v30, v[192:193], off offset:512
	global_load_ushort v31, v[194:195], off offset:512
	global_load_ushort v108, v[70:71], off
	global_load_ushort v109, v[72:73], off
	global_load_ushort v112, v[192:193], off offset:1024
	global_load_ushort v113, v[194:195], off offset:1024
	global_load_ushort v114, v[74:75], off
	global_load_ushort v115, v[76:77], off
	global_load_ushort v110, v[192:193], off offset:1536
	global_load_ushort v111, v[194:195], off offset:1536
	global_load_ushort v116, v[78:79], off
	global_load_ushort v117, v[80:81], off
	s_waitcnt vmcnt(24)
	global_load_ushort v120, v[192:193], off offset:2048
	global_load_ushort v121, v[194:195], off offset:2048
	global_load_ushort v122, v[82:83], off
	global_load_ushort v123, v[84:85], off
	global_load_ushort v118, v[192:193], off offset:2560
	global_load_ushort v119, v[194:195], off offset:2560
	global_load_ushort v124, v[86:87], off
	global_load_ushort v125, v[88:89], off
	global_load_ushort v128, v[192:193], off offset:3072
	global_load_ushort v129, v[194:195], off offset:3072
	global_load_ushort v130, v[90:91], off
	global_load_ushort v131, v[92:93], off
	global_load_ushort v126, v[192:193], off offset:3584
	global_load_ushort v127, v[194:195], off offset:3584
	global_load_ushort v132, v[94:95], off
	global_load_ushort v133, v[96:97], off
	s_waitcnt vmcnt(0)
; __device__ __forceinline__ unsigned pk2(float lo, float hi) { const f32x2cv v = {lo, hi}; return __builtin_bit_cast(unsigned, __builtin_convertvector(v, bf16x2cv)); }
; __device__ __forceinline__ unsigned f2bf(float f) { return pk2(f, 0.f); }
; template <bool LAT>
; __device__ __forceinline__ void hyconv_unit(const Frame& F, LAS f32x2v* X, const TwHalf tw, LAS bf16* OUT, const float* skip, bf16* MIX, int u) {
;     ...
;                   for (int r = 0; r < 16; ++r) { g[r] = (f32x2v){0.f, 0.f}; zp[r] = g[r]; if (act) { g[r] = (f32x2v){bf2f(g0[r * L]), bf2f(g1[r * L])}; zp[r] = (f32x2v){bf2f(v0[r * L]), bf2f(v1[r * L])}; } } }
;                 f32x2v z[16];
; #pragma unroll
;                 for (int r = 0; r < 16; ++r) { z[r] = g[r] * (X[PADI(F.tid + 512 * r)] + zp[r] * skip[ord * 256 + c0 + r]); }
;                 if (ord == 0) { bf16* v0 = H0 + (size_t)(512 + c0) * L + n; bf16* v1 = H1 + (size_t)(512 + c0) * L + n;
; #pragma unroll
;                     for (int r = 0; r < 16; ++r) { if (act) { v0[r * L] = (bf16)f2bf(z[r].x); v1[r * L] = (bf16)f2bf(z[r].y); } X[PADI(F.tid + 512 * r)] = z[r]; } }
;                 else if (act) {
;                     v4u oa, ob, oc, od;
;                     oa.x = pk2(z[0].x, z[1].x); oa.y = pk2(z[2].x, z[3].x); oa.z = pk2(z[4].x, z[5].x); oa.w = pk2(z[6].x, z[7].x); ob.x = pk2(z[8].x, z[9].x); ob.y = pk2(z[10].x, z[11].x); ob.z = pk2(z[12].x, z[13].x); ob.w = pk2(z[14].x, z[15].x);
;                     oc.x = pk2(z[0].y, z[1].y); oc.y = pk2(z[2].y, z[3].y); oc.z = pk2(z[4].y, z[5].y); oc.w = pk2(z[6].y, z[7].y); od.x = pk2(z[8].y, z[9].y); od.y = pk2(z[10].y, z[11].y); od.z = pk2(z[12].y, z[13].y); od.w = pk2(z[14].y, z[15].y);
;                     bf16* m0 = MIX + (size_t)(rowb + n) * 1024 + c0; bf16* m1 = m0 + (size_t)L * 1024;
;                     *(v4u*)m0 = oa; *(v4u*)(m0 + 8) = ob; *(v4u*)m1 = oc; *(v4u*)(m1 + 8) = od; }
	v_lshlrev_b32_e32 v2, 16, v2
	v_lshlrev_b32_e32 v3, 16, v3
	v_lshlrev_b32_e32 v4, 16, v4
	v_lshlrev_b32_e32 v5, 16, v5
	v_lshlrev_b32_e32 v0, 16, v0
	v_lshlrev_b32_e32 v1, 16, v1
	v_lshlrev_b32_e32 v6, 16, v6
	v_lshlrev_b32_e32 v7, 16, v7
	v_lshlrev_b32_e32 v10, 16, v10
	v_lshlrev_b32_e32 v11, 16, v11
	v_lshlrev_b32_e32 v12, 16, v12
	v_lshlrev_b32_e32 v13, 16, v13
	v_lshlrev_b32_e32 v8, 16, v8
	v_lshlrev_b32_e32 v9, 16, v9
	v_lshlrev_b32_e32 v14, 16, v14
	v_lshlrev_b32_e32 v15, 16, v15
	v_lshlrev_b32_e32 v18, 16, v18
	v_lshlrev_b32_e32 v19, 16, v19
	v_lshlrev_b32_e32 v20, 16, v20
	v_lshlrev_b32_e32 v21, 16, v21
	v_lshlrev_b32_e32 v16, 16, v16
	v_lshlrev_b32_e32 v17, 16, v17
	v_lshlrev_b32_e32 v22, 16, v22
	v_lshlrev_b32_e32 v23, 16, v23
	v_lshlrev_b32_e32 v26, 16, v26
	v_lshlrev_b32_e32 v27, 16, v27
	v_lshlrev_b32_e32 v28, 16, v28
	v_lshlrev_b32_e32 v29, 16, v29
	v_lshlrev_b32_e32 v24, 16, v24
	v_lshlrev_b32_e32 v25, 16, v25
	v_lshlrev_b32_e32 v98, 16, v98
	v_lshlrev_b32_e32 v99, 16, v99
	v_lshlrev_b32_e32 v100, 16, v100
	v_lshlrev_b32_e32 v101, 16, v101
	v_lshlrev_b32_e32 v106, 16, v106
	v_lshlrev_b32_e32 v107, 16, v107
	v_lshlrev_b32_e32 v30, 16, v30
	v_lshlrev_b32_e32 v31, 16, v31
	v_lshlrev_b32_e32 v108, 16, v108
	v_lshlrev_b32_e32 v109, 16, v109
	v_lshlrev_b32_e32 v112, 16, v112
	v_lshlrev_b32_e32 v113, 16, v113
	v_lshlrev_b32_e32 v114, 16, v114
	v_lshlrev_b32_e32 v115, 16, v115
	v_lshlrev_b32_e32 v110, 16, v110
	v_lshlrev_b32_e32 v111, 16, v111
	v_lshlrev_b32_e32 v116, 16, v116
	v_lshlrev_b32_e32 v117, 16, v117
	v_lshlrev_b32_e32 v120, 16, v120
	v_lshlrev_b32_e32 v121, 16, v121
	v_lshlrev_b32_e32 v122, 16, v122
	v_lshlrev_b32_e32 v123, 16, v123
	v_lshlrev_b32_e32 v118, 16, v118
	v_lshlrev_b32_e32 v119, 16, v119
	v_lshlrev_b32_e32 v124, 16, v124
	v_lshlrev_b32_e32 v125, 16, v125
	v_lshlrev_b32_e32 v128, 16, v128
	v_lshlrev_b32_e32 v129, 16, v129
	v_lshlrev_b32_e32 v130, 16, v130
	v_lshlrev_b32_e32 v131, 16, v131
	v_lshlrev_b32_e32 v126, 16, v126
	v_lshlrev_b32_e32 v127, 16, v127
	v_lshlrev_b32_e32 v132, 16, v132
	v_lshlrev_b32_e32 v133, 16, v133
	s_or_b64 exec, exec, s[0:1]
	s_mov_b32 s15, s91
	s_xor_b64 s[0:1], s[20:21], -1
	s_lshl_b64 s[2:3], s[14:15], 2
	s_add_u32 s2, s6, s2
	s_addc_u32 s3, s7, s3
	ds_read_b64 v[190:191], v140
	global_load_dwordx4 v[176:179], v181, s[2:3] offset:48
	global_load_dwordx4 v[182:185], v181, s[2:3] offset:32
	global_load_dwordx4 v[186:189], v181, s[2:3] offset:16
	global_load_dwordx4 v[102:105], v181, s[2:3]
	s_mov_b64 s[2:3], -1
	s_and_b64 vcc, exec, s[0:1]
	s_waitcnt vmcnt(0) lgkmcnt(0)
	v_pk_fma_f32 v[4:5], v[4:5], v[102:103], v[190:191] op_sel_hi:[1,0,1]
	s_nop 0
	v_pk_mul_f32 v[2:3], v[2:3], v[4:5]
	ds_read_b64 v[4:5], v141 offset:4096
	s_waitcnt lgkmcnt(0)
	v_pk_fma_f32 v[4:5], v[6:7], v[102:103], v[4:5] op_sel:[0,1,0]
	s_nop 0
	v_pk_mul_f32 v[102:103], v[0:1], v[4:5]
	ds_read_b64 v[0:1], v142 offset:8192
	v_mov_b32_e32 v6, v105
	s_waitcnt lgkmcnt(0)
	v_pk_fma_f32 v[0:1], v[12:13], v[104:105], v[0:1] op_sel_hi:[1,0,1]
	s_nop 0
	v_pk_mul_f32 v[4:5], v[10:11], v[0:1]
	ds_read_b64 v[0:1], v143 offset:12288
	v_mov_b32_e32 v10, v189
	s_waitcnt lgkmcnt(0)
	v_pk_fma_f32 v[0:1], v[14:15], v[6:7], v[0:1] op_sel_hi:[1,0,1]
	s_nop 0
	v_pk_mul_f32 v[104:105], v[8:9], v[0:1]
	ds_read_b64 v[0:1], v144 offset:16384
	ds_read_b64 v[6:7], v145 offset:20480
	s_waitcnt lgkmcnt(1)
	v_pk_fma_f32 v[0:1], v[20:21], v[186:187], v[0:1] op_sel_hi:[1,0,1]
	s_waitcnt lgkmcnt(0)
	v_pk_fma_f32 v[6:7], v[22:23], v[186:187], v[6:7] op_sel:[0,1,0]
	v_pk_mul_f32 v[0:1], v[18:19], v[0:1]
	v_pk_mul_f32 v[12:13], v[16:17], v[6:7]
	ds_read_b64 v[6:7], v146 offset:24576
	v_mov_b32_e32 v18, v185
	s_waitcnt lgkmcnt(0)
	v_pk_fma_f32 v[6:7], v[28:29], v[188:189], v[6:7] op_sel_hi:[1,0,1]
	s_nop 0
	v_pk_mul_f32 v[8:9], v[26:27], v[6:7]
	ds_read_b64 v[6:7], v147 offset:28672
	ds_read_b64 v[26:27], v155 offset:61440
	v_mov_b32_e32 v28, v179
	s_waitcnt lgkmcnt(1)
	v_pk_fma_f32 v[6:7], v[98:99], v[10:11], v[6:7] op_sel_hi:[1,0,1]
	s_nop 0
	v_pk_mul_f32 v[22:23], v[24:25], v[6:7]
	ds_read_b64 v[6:7], v148 offset:32768
	ds_read_b64 v[10:11], v149 offset:36864
	s_waitcnt lgkmcnt(2)
	v_pk_fma_f32 v[26:27], v[132:133], v[28:29], v[26:27] op_sel_hi:[1,0,1]
	s_waitcnt lgkmcnt(1)
	v_pk_fma_f32 v[6:7], v[106:107], v[182:183], v[6:7] op_sel_hi:[1,0,1]
	s_waitcnt lgkmcnt(0)
	v_pk_fma_f32 v[10:11], v[108:109], v[182:183], v[10:11] op_sel:[0,1,0]
	v_pk_mul_f32 v[6:7], v[100:101], v[6:7]
	v_pk_mul_f32 v[16:17], v[30:31], v[10:11]
	ds_read_b64 v[10:11], v150 offset:40960
	v_pk_mul_f32 v[26:27], v[126:127], v[26:27]
	s_waitcnt lgkmcnt(0)
	v_pk_fma_f32 v[10:11], v[114:115], v[184:185], v[10:11] op_sel_hi:[1,0,1]
	s_nop 0
	v_pk_mul_f32 v[14:15], v[112:113], v[10:11]
	ds_read_b64 v[10:11], v151 offset:45056
	s_waitcnt lgkmcnt(0)
	v_pk_fma_f32 v[10:11], v[116:117], v[18:19], v[10:11] op_sel_hi:[1,0,1]
	s_nop 0
	v_pk_mul_f32 v[24:25], v[110:111], v[10:11]
	ds_read_b64 v[10:11], v152 offset:49152
	ds_read_b64 v[18:19], v153 offset:53248
	s_waitcnt lgkmcnt(1)
	v_pk_fma_f32 v[10:11], v[122:123], v[176:177], v[10:11] op_sel_hi:[1,0,1]
	s_waitcnt lgkmcnt(0)
	v_pk_fma_f32 v[18:19], v[124:125], v[176:177], v[18:19] op_sel:[0,1,0]
	v_pk_mul_f32 v[10:11], v[120:121], v[10:11]
	v_pk_mul_f32 v[20:21], v[118:119], v[18:19]
	ds_read_b64 v[18:19], v154 offset:57344
	s_waitcnt lgkmcnt(0)
	v_pk_fma_f32 v[18:19], v[130:131], v[178:179], v[18:19] op_sel_hi:[1,0,1]
	s_nop 0
	v_pk_mul_f32 v[18:19], v[128:129], v[18:19]
	s_cbranch_vccz .LBB0_883
	s_and_saveexec_b64 s[2:3], s[38:39]
	s_cbranch_execz .LBB0_882
	v_cvt_pk_bf16_f32 v28, v2, v102
	v_cvt_pk_bf16_f32 v29, v4, v104
	v_cvt_pk_bf16_f32 v30, v0, v12
	v_cvt_pk_bf16_f32 v31, v8, v22
	v_cvt_pk_bf16_f32 v98, v6, v16
	v_cvt_pk_bf16_f32 v99, v14, v24
	v_cvt_pk_bf16_f32 v100, v10, v20
	v_cvt_pk_bf16_f32 v101, v18, v26
	v_cvt_pk_bf16_f32 v106, v3, v103
	v_cvt_pk_bf16_f32 v107, v5, v105
	v_cvt_pk_bf16_f32 v108, v1, v13
	v_cvt_pk_bf16_f32 v109, v9, v23
	v_cvt_pk_bf16_f32 v110, v7, v17
	v_cvt_pk_bf16_f32 v111, v15, v25
	v_cvt_pk_bf16_f32 v112, v11, v21
	v_cvt_pk_bf16_f32 v113, v19, v27
	global_store_dwordx4 v[58:59], v[28:31], off
	global_store_dwordx4 v[58:59], v[98:101], off offset:16
	global_store_dwordx4 v[60:61], v[106:109], off
	global_store_dwordx4 v[64:65], v[110:113], off
